# GEMM epilogue output stores of P8/P9/P11/P14 nt
# speedup vs baseline: 1.0137x; 1.0063x over previous
.LBB0_1121:
	s_lshl_b32 s4, s63, 8
	v_mov_b32_e32 v108, v0
	s_add_i32 s4, s4, s58
	v_and_b32_e32 v198, 64, v250
	v_and_or_b32 v216, v108, 15, s4
	s_lshl_b32 s4, s56, 8
	v_bfe_u32 v196, v108, 4, 2
	s_or_b32 s4, s4, s59
	v_lshl_or_b32 v214, v196, 3, s4
	v_ashrrev_i32_e32 v215, 31, v214
	v_ashrrev_i32_e32 v217, 31, v216
	v_lshlrev_b64 v[232:233], 1, v[214:215]
	v_lshl_add_u64 v[118:119], s[14:15], 0, v[232:233]
	v_lshlrev_b64 v[234:235], 11, v[216:217]
	v_lshl_add_u64 v[128:129], v[118:119], 0, v[234:235]
	global_load_dwordx4 v[192:195], v[128:129], off
	global_load_dwordx4 v[188:191], v[128:129], off offset:256
	v_or_b32_e32 v228, 16, v216
	v_ashrrev_i32_e32 v229, 31, v228
	v_or_b32_e32 v224, 32, v216
	v_ashrrev_i32_e32 v225, 31, v224
	v_or_b32_e32 v220, 48, v216
	v_lshlrev_b64 v[230:231], 11, v[228:229]
	v_ashrrev_i32_e32 v221, 31, v220
	v_lshl_add_u64 v[128:129], v[118:119], 0, v[230:231]
	v_lshlrev_b64 v[226:227], 11, v[224:225]
	v_add_u32_e32 v218, 0x80, v216
	v_add_u32_e32 v108, 0x90, v216
	global_load_dwordx4 v[184:187], v[128:129], off
	global_load_dwordx4 v[180:183], v[128:129], off offset:256
	v_lshl_add_u64 v[128:129], v[118:119], 0, v[226:227]
	v_lshlrev_b64 v[222:223], 11, v[220:221]
	v_ashrrev_i32_e32 v219, 31, v218
	v_ashrrev_i32_e32 v109, 31, v108
	global_load_dwordx4 v[176:179], v[128:129], off
	global_load_dwordx4 v[172:175], v[128:129], off offset:256
	v_lshl_add_u64 v[128:129], v[118:119], 0, v[222:223]
	v_add_u32_e32 v110, 0xa0, v216
	global_load_dwordx4 v[168:171], v[128:129], off
	global_load_dwordx4 v[164:167], v[128:129], off offset:256
	v_lshlrev_b64 v[128:129], 11, v[218:219]
	v_lshlrev_b64 v[108:109], 11, v[108:109]
	v_ashrrev_i32_e32 v111, 31, v110
	v_lshl_add_u64 v[128:129], v[118:119], 0, v[128:129]
	v_lshl_add_u64 v[108:109], v[118:119], 0, v[108:109]
	v_add_u32_e32 v116, 0xb0, v216
	global_load_dwordx4 v[160:163], v[128:129], off
	global_load_dwordx4 v[156:159], v[128:129], off offset:256
	global_load_dwordx4 v[152:155], v[108:109], off
	global_load_dwordx4 v[148:151], v[108:109], off offset:256
	v_lshlrev_b64 v[108:109], 11, v[110:111]
	v_ashrrev_i32_e32 v117, 31, v116
	v_lshl_add_u64 v[108:109], v[118:119], 0, v[108:109]
	global_load_dwordx4 v[136:139], v[108:109], off
	global_load_dwordx4 v[128:131], v[108:109], off offset:256
	v_lshlrev_b64 v[108:109], 11, v[116:117]
	v_lshl_add_u64 v[108:109], v[118:119], 0, v[108:109]
	global_load_dwordx4 v[116:119], v[108:109], off
	s_nop 0
	global_load_dwordx4 v[108:111], v[108:109], off offset:256
	v_xor_b32_e32 v197, 16, v250
	v_add_u32_e32 v198, 64, v198
	v_cmp_lt_i32_e32 vcc, v197, v198
	s_lshl_b32 s44, s56, 2
	s_ashr_i32 s45, s44, 31
	v_cndmask_b32_e32 v197, v250, v197, vcc
	v_lshlrev_b32_e32 v237, 2, v197
	v_xor_b32_e32 v197, 32, v250
	v_cmp_lt_i32_e32 vcc, v197, v198
	s_waitcnt vmcnt(0)
	v_lshlrev_b32_e32 v198, 16, v194
	v_cndmask_b32_e32 v197, v250, v197, vcc
	v_lshlrev_b32_e32 v238, 2, v197
	v_cmp_eq_u32_e32 vcc, 0, v196
	v_lshlrev_b32_e32 v196, 16, v192
	v_and_b32_e32 v197, 0xffff0000, v192
	v_lshlrev_b32_e32 v192, 16, v193
	v_and_b32_e32 v193, 0xffff0000, v193
	v_and_b32_e32 v199, 0xffff0000, v194
	v_lshlrev_b32_e32 v194, 16, v195
	v_and_b32_e32 v195, 0xffff0000, v195
	v_pk_add_f32 v[144:145], v[144:145], v[196:197]
	v_pk_add_f32 v[146:147], v[146:147], v[192:193]
	v_pk_add_f32 v[192:193], v[142:143], v[194:195]
	v_pk_add_f32 v[142:143], v[140:141], v[198:199]
	v_cvt_pk_bf16_f32 v140, v144, v145
	v_lshl_add_u64 v[144:145], s[14:15], 0, v[234:235]
	v_cvt_pk_bf16_f32 v141, v146, v147
	v_cvt_pk_bf16_f32 v142, v142, v143
	v_cvt_pk_bf16_f32 v143, v192, v193
	v_lshl_add_u64 v[144:145], v[144:145], 0, v[232:233]
	global_store_dwordx4 v[144:145], v[140:143], off nt
	v_lshlrev_b32_e32 v146, 16, v140
	v_lshlrev_b32_e32 v147, 16, v141
	v_and_b32_e32 v140, 0xffff0000, v140
	v_and_b32_e32 v141, 0xffff0000, v141
	v_mul_f32_e32 v140, v140, v140
	v_mul_f32_e32 v141, v141, v141
	v_lshlrev_b32_e32 v192, 16, v142
	v_and_b32_e32 v142, 0xffff0000, v142
	v_lshlrev_b32_e32 v193, 16, v143
	v_and_b32_e32 v143, 0xffff0000, v143
	v_fmac_f32_e32 v140, v146, v146
	v_fmac_f32_e32 v141, v147, v147
	v_add_f32_e32 v140, v140, v141
	v_mul_f32_e32 v141, v142, v142
	v_mul_f32_e32 v142, v143, v143
	v_fmac_f32_e32 v141, v192, v192
	v_fmac_f32_e32 v142, v193, v193
	v_add_f32_e32 v141, v141, v142
	v_add_f32_e32 v192, v140, v141
	v_lshlrev_b32_e32 v140, 16, v188
	v_and_b32_e32 v141, 0xffff0000, v188
	v_lshlrev_b32_e32 v142, 16, v189
	v_and_b32_e32 v143, 0xffff0000, v189
	v_lshlrev_b32_e32 v146, 16, v190
	v_and_b32_e32 v147, 0xffff0000, v190
	v_lshlrev_b32_e32 v188, 16, v191
	v_and_b32_e32 v189, 0xffff0000, v191
	v_pk_add_f32 v[134:135], v[134:135], v[142:143]
	v_pk_add_f32 v[132:133], v[132:133], v[140:141]
	v_pk_add_f32 v[140:141], v[126:127], v[188:189]
	v_pk_add_f32 v[126:127], v[124:125], v[146:147]
	v_cvt_pk_bf16_f32 v124, v132, v133
	v_cvt_pk_bf16_f32 v125, v134, v135
	v_cvt_pk_bf16_f32 v126, v126, v127
	v_cvt_pk_bf16_f32 v127, v140, v141
	global_store_dwordx4 v[144:145], v[124:127], off offset:256 nt
	v_lshlrev_b32_e32 v132, 16, v124
	v_lshlrev_b32_e32 v133, 16, v125
	v_and_b32_e32 v124, 0xffff0000, v124
	v_and_b32_e32 v125, 0xffff0000, v125
	v_mul_f32_e32 v124, v124, v124
	v_mul_f32_e32 v125, v125, v125
	v_lshlrev_b32_e32 v134, 16, v126
	v_and_b32_e32 v126, 0xffff0000, v126
	v_lshlrev_b32_e32 v135, 16, v127
	v_and_b32_e32 v127, 0xffff0000, v127
	v_fmac_f32_e32 v124, v132, v132
	v_fmac_f32_e32 v125, v133, v133
	v_add_f32_e32 v124, v124, v125
	v_mul_f32_e32 v125, v126, v126
	v_mul_f32_e32 v126, v127, v127
	v_fmac_f32_e32 v125, v134, v134
	v_fmac_f32_e32 v126, v135, v135
	v_add_f32_e32 v125, v125, v126
	v_add_f32_e32 v124, v124, v125
	v_add_f32_e32 v124, v192, v124
	ds_bpermute_b32 v125, v237, v124
	s_waitcnt lgkmcnt(0)
	v_add_f32_e32 v124, v124, v125
	ds_bpermute_b32 v125, v238, v124
	s_and_saveexec_b64 s[4:5], vcc
	s_cbranch_execz .LBB0_1123
	v_lshlrev_b64 v[126:127], 6, v[216:217]
	v_lshl_add_u64 v[126:127], s[18:19], 0, v[126:127]
	v_lshl_add_u64 v[126:127], s[44:45], 2, v[126:127]
	s_lshl_b32 s56, s53, 2
	v_lshl_add_u64 v[126:127], v[126:127], 0, s[56:57]
	s_waitcnt lgkmcnt(0)
	v_add_f32_e32 v124, v124, v125
	global_store_dword v[126:127], v124, off
.LBB0_1123:
	s_or_b64 exec, exec, s[4:5]
	v_lshlrev_b32_e32 v124, 16, v184
	s_waitcnt lgkmcnt(0)
	v_and_b32_e32 v125, 0xffff0000, v184
	v_lshlrev_b32_e32 v126, 16, v185
	v_and_b32_e32 v127, 0xffff0000, v185
	v_lshlrev_b32_e32 v132, 16, v186
	v_and_b32_e32 v133, 0xffff0000, v186
	v_lshlrev_b32_e32 v134, 16, v187
	v_and_b32_e32 v135, 0xffff0000, v187
	v_pk_add_f32 v[120:121], v[120:121], v[124:125]
	v_pk_add_f32 v[122:123], v[122:123], v[126:127]
	v_pk_add_f32 v[124:125], v[114:115], v[134:135]
	v_pk_add_f32 v[114:115], v[112:113], v[132:133]
	v_cvt_pk_bf16_f32 v112, v120, v121
	v_cvt_pk_bf16_f32 v113, v122, v123
	v_and_b32_e32 v121, 0xffff0000, v112
	v_lshlrev_b32_e32 v120, 16, v112
	v_and_b32_e32 v123, 0xffff0000, v113
	v_mul_f32_e32 v121, v121, v121
	v_cvt_pk_bf16_f32 v114, v114, v115
	v_cvt_pk_bf16_f32 v115, v124, v125
	v_lshlrev_b32_e32 v122, 16, v113
	v_fmac_f32_e32 v121, v120, v120
	v_mul_f32_e32 v120, v123, v123
	v_and_b32_e32 v125, 0xffff0000, v114
	v_and_b32_e32 v127, 0xffff0000, v115
	v_fmac_f32_e32 v120, v122, v122
	v_lshlrev_b32_e32 v124, 16, v114
	v_lshlrev_b32_e32 v126, 16, v115
	v_add_f32_e32 v120, v121, v120
	v_mul_f32_e32 v121, v125, v125
	v_mul_f32_e32 v122, v127, v127
	v_fmac_f32_e32 v121, v124, v124
	v_fmac_f32_e32 v122, v126, v126
	v_add_f32_e32 v121, v121, v122
	v_add_f32_e32 v132, v120, v121
	v_lshlrev_b32_e32 v120, 16, v180
	v_and_b32_e32 v121, 0xffff0000, v180
	v_lshlrev_b32_e32 v122, 16, v181
	v_and_b32_e32 v123, 0xffff0000, v181
	v_lshlrev_b32_e32 v124, 16, v182
	v_and_b32_e32 v125, 0xffff0000, v182
	v_lshlrev_b32_e32 v126, 16, v183
	v_and_b32_e32 v127, 0xffff0000, v183
	v_pk_add_f32 v[104:105], v[104:105], v[120:121]
	v_pk_add_f32 v[106:107], v[106:107], v[122:123]
	v_pk_add_f32 v[120:121], v[102:103], v[126:127]
	v_pk_add_f32 v[100:101], v[100:101], v[124:125]
	v_cvt_pk_bf16_f32 v102, v104, v105
	v_cvt_pk_bf16_f32 v103, v106, v107
	v_cvt_pk_bf16_f32 v104, v100, v101
	v_and_b32_e32 v101, 0xffff0000, v102
	v_lshlrev_b32_e32 v100, 16, v102
	v_and_b32_e32 v107, 0xffff0000, v103
	v_mul_f32_e32 v101, v101, v101
	v_cvt_pk_bf16_f32 v105, v120, v121
	v_lshlrev_b32_e32 v106, 16, v103
	v_fmac_f32_e32 v101, v100, v100
	v_mul_f32_e32 v100, v107, v107
	v_and_b32_e32 v121, 0xffff0000, v104
	v_and_b32_e32 v123, 0xffff0000, v105
	v_fmac_f32_e32 v100, v106, v106
	v_lshlrev_b32_e32 v120, 16, v104
	v_lshlrev_b32_e32 v122, 16, v105
	v_add_f32_e32 v100, v101, v100
	v_mul_f32_e32 v101, v121, v121
	v_mul_f32_e32 v106, v123, v123
	v_fmac_f32_e32 v101, v120, v120
	v_fmac_f32_e32 v106, v122, v122
	v_add_f32_e32 v101, v101, v106
	v_add_f32_e32 v100, v100, v101
	v_add_f32_e32 v100, v132, v100
	ds_bpermute_b32 v101, v237, v100
	v_lshl_add_u64 v[106:107], s[14:15], 0, v[230:231]
	v_lshl_add_u64 v[106:107], v[214:215], 1, v[106:107]
	global_store_dwordx4 v[106:107], v[112:115], off nt
	global_store_dwordx4 v[106:107], v[102:105], off offset:256 nt
	s_waitcnt lgkmcnt(0)
	v_add_f32_e32 v100, v100, v101
	ds_bpermute_b32 v101, v238, v100
	s_and_saveexec_b64 s[4:5], vcc
	s_cbranch_execz .LBB0_1125
	v_lshlrev_b64 v[102:103], 6, v[228:229]
	v_lshl_add_u64 v[102:103], s[18:19], 0, v[102:103]
	v_lshl_add_u64 v[102:103], s[44:45], 2, v[102:103]
	s_lshl_b32 s56, s53, 2
	v_lshl_add_u64 v[102:103], v[102:103], 0, s[56:57]
	s_waitcnt lgkmcnt(0)
	v_add_f32_e32 v100, v100, v101
	global_store_dword v[102:103], v100, off
.LBB0_1125:
	s_or_b64 exec, exec, s[4:5]
	v_lshlrev_b32_e32 v100, 16, v176
	s_waitcnt lgkmcnt(0)
	v_and_b32_e32 v101, 0xffff0000, v176
	v_lshlrev_b32_e32 v102, 16, v177
	v_and_b32_e32 v103, 0xffff0000, v177
	v_lshlrev_b32_e32 v104, 16, v178
	v_and_b32_e32 v105, 0xffff0000, v178
	v_lshlrev_b32_e32 v106, 16, v179
	v_and_b32_e32 v107, 0xffff0000, v179
	v_pk_add_f32 v[96:97], v[96:97], v[100:101]
	v_pk_add_f32 v[98:99], v[98:99], v[102:103]
	v_pk_add_f32 v[100:101], v[94:95], v[106:107]
	v_pk_add_f32 v[94:95], v[92:93], v[104:105]
	v_cvt_pk_bf16_f32 v92, v96, v97
	v_cvt_pk_bf16_f32 v93, v98, v99
	v_and_b32_e32 v97, 0xffff0000, v92
	v_lshlrev_b32_e32 v96, 16, v92
	v_and_b32_e32 v99, 0xffff0000, v93
	v_mul_f32_e32 v97, v97, v97
	v_cvt_pk_bf16_f32 v94, v94, v95
	v_cvt_pk_bf16_f32 v95, v100, v101
	v_lshlrev_b32_e32 v98, 16, v93
	v_fmac_f32_e32 v97, v96, v96
	v_mul_f32_e32 v96, v99, v99
	v_and_b32_e32 v101, 0xffff0000, v94
	v_and_b32_e32 v103, 0xffff0000, v95
	v_fmac_f32_e32 v96, v98, v98
	v_lshlrev_b32_e32 v100, 16, v94
	v_lshlrev_b32_e32 v102, 16, v95
	v_add_f32_e32 v96, v97, v96
	v_mul_f32_e32 v97, v101, v101
	v_mul_f32_e32 v98, v103, v103
	v_fmac_f32_e32 v97, v100, v100
	v_fmac_f32_e32 v98, v102, v102
	v_add_f32_e32 v97, v97, v98
	v_add_f32_e32 v104, v96, v97
	v_lshlrev_b32_e32 v96, 16, v172
	v_and_b32_e32 v97, 0xffff0000, v172
	v_lshlrev_b32_e32 v98, 16, v173
	v_and_b32_e32 v99, 0xffff0000, v173
	v_lshlrev_b32_e32 v100, 16, v174
	v_and_b32_e32 v101, 0xffff0000, v174
	v_lshlrev_b32_e32 v102, 16, v175
	v_and_b32_e32 v103, 0xffff0000, v175
	v_pk_add_f32 v[88:89], v[88:89], v[96:97]
	v_pk_add_f32 v[90:91], v[90:91], v[98:99]
	v_pk_add_f32 v[96:97], v[86:87], v[102:103]
	v_pk_add_f32 v[84:85], v[84:85], v[100:101]
	v_cvt_pk_bf16_f32 v86, v88, v89
	v_cvt_pk_bf16_f32 v87, v90, v91
	v_cvt_pk_bf16_f32 v88, v84, v85
	v_and_b32_e32 v85, 0xffff0000, v86
	v_lshlrev_b32_e32 v84, 16, v86
	v_and_b32_e32 v91, 0xffff0000, v87
	v_mul_f32_e32 v85, v85, v85
	v_cvt_pk_bf16_f32 v89, v96, v97
	v_lshlrev_b32_e32 v90, 16, v87
	v_fmac_f32_e32 v85, v84, v84
	v_mul_f32_e32 v84, v91, v91
	v_and_b32_e32 v97, 0xffff0000, v88
	v_and_b32_e32 v99, 0xffff0000, v89
	v_fmac_f32_e32 v84, v90, v90
	v_lshlrev_b32_e32 v96, 16, v88
	v_lshlrev_b32_e32 v98, 16, v89
	v_add_f32_e32 v84, v85, v84
	v_mul_f32_e32 v85, v97, v97
	v_mul_f32_e32 v90, v99, v99
	v_fmac_f32_e32 v85, v96, v96
	v_fmac_f32_e32 v90, v98, v98
	v_add_f32_e32 v85, v85, v90
	v_add_f32_e32 v84, v84, v85
	v_add_f32_e32 v84, v104, v84
	ds_bpermute_b32 v85, v237, v84
	v_lshl_add_u64 v[90:91], s[14:15], 0, v[226:227]
	v_lshl_add_u64 v[90:91], v[214:215], 1, v[90:91]
	global_store_dwordx4 v[90:91], v[92:95], off nt
	global_store_dwordx4 v[90:91], v[86:89], off offset:256 nt
	s_waitcnt lgkmcnt(0)
	v_add_f32_e32 v84, v84, v85
	ds_bpermute_b32 v85, v238, v84
	s_and_saveexec_b64 s[4:5], vcc
	s_mov_b32 s76, 0xe000
	s_movk_i32 s75, 0x3400
	v_readlane_b32 s74, v255, 38
	s_cbranch_execz .LBB0_1127
	v_lshlrev_b64 v[86:87], 6, v[224:225]
	v_lshl_add_u64 v[86:87], s[18:19], 0, v[86:87]
	v_lshl_add_u64 v[86:87], s[44:45], 2, v[86:87]
	s_lshl_b32 s56, s53, 2
	v_lshl_add_u64 v[86:87], v[86:87], 0, s[56:57]
	s_waitcnt lgkmcnt(0)
	v_add_f32_e32 v84, v84, v85
	global_store_dword v[86:87], v84, off
.LBB0_1127:
	s_or_b64 exec, exec, s[4:5]
	v_lshlrev_b32_e32 v84, 16, v168
	s_waitcnt lgkmcnt(0)
	v_and_b32_e32 v85, 0xffff0000, v168
	v_lshlrev_b32_e32 v86, 16, v169
	v_and_b32_e32 v87, 0xffff0000, v169
	v_lshlrev_b32_e32 v88, 16, v170
	v_and_b32_e32 v89, 0xffff0000, v170
	v_lshlrev_b32_e32 v90, 16, v171
	v_and_b32_e32 v91, 0xffff0000, v171
	v_pk_add_f32 v[80:81], v[80:81], v[84:85]
	v_pk_add_f32 v[82:83], v[82:83], v[86:87]
	v_pk_add_f32 v[84:85], v[78:79], v[90:91]
	v_pk_add_f32 v[78:79], v[76:77], v[88:89]
	v_cvt_pk_bf16_f32 v76, v80, v81
	v_cvt_pk_bf16_f32 v77, v82, v83
	v_and_b32_e32 v81, 0xffff0000, v76
	v_lshlrev_b32_e32 v80, 16, v76
	v_and_b32_e32 v83, 0xffff0000, v77
	v_mul_f32_e32 v81, v81, v81
	v_cvt_pk_bf16_f32 v78, v78, v79
	v_cvt_pk_bf16_f32 v79, v84, v85
	v_lshlrev_b32_e32 v82, 16, v77
	v_fmac_f32_e32 v81, v80, v80
	v_mul_f32_e32 v80, v83, v83
	v_and_b32_e32 v85, 0xffff0000, v78
	v_and_b32_e32 v87, 0xffff0000, v79
	v_fmac_f32_e32 v80, v82, v82
	v_lshlrev_b32_e32 v84, 16, v78
	v_lshlrev_b32_e32 v86, 16, v79
	v_add_f32_e32 v80, v81, v80
	v_mul_f32_e32 v81, v85, v85
	v_mul_f32_e32 v82, v87, v87
	v_fmac_f32_e32 v81, v84, v84
	v_fmac_f32_e32 v82, v86, v86
	v_add_f32_e32 v81, v81, v82
	v_add_f32_e32 v88, v80, v81
	v_lshlrev_b32_e32 v80, 16, v164
	v_and_b32_e32 v81, 0xffff0000, v164
	v_lshlrev_b32_e32 v82, 16, v165
	v_and_b32_e32 v83, 0xffff0000, v165
	v_lshlrev_b32_e32 v84, 16, v166
	v_and_b32_e32 v85, 0xffff0000, v166
	v_lshlrev_b32_e32 v86, 16, v167
	v_and_b32_e32 v87, 0xffff0000, v167
	v_pk_add_f32 v[72:73], v[72:73], v[80:81]
	v_pk_add_f32 v[74:75], v[74:75], v[82:83]
	v_pk_add_f32 v[80:81], v[70:71], v[86:87]
	v_pk_add_f32 v[68:69], v[68:69], v[84:85]
	v_cvt_pk_bf16_f32 v70, v72, v73
	v_cvt_pk_bf16_f32 v71, v74, v75
	v_cvt_pk_bf16_f32 v72, v68, v69
	v_and_b32_e32 v69, 0xffff0000, v70
	v_lshlrev_b32_e32 v68, 16, v70
	v_and_b32_e32 v75, 0xffff0000, v71
	v_mul_f32_e32 v69, v69, v69
	v_cvt_pk_bf16_f32 v73, v80, v81
	v_lshlrev_b32_e32 v74, 16, v71
	v_fmac_f32_e32 v69, v68, v68
	v_mul_f32_e32 v68, v75, v75
	v_and_b32_e32 v81, 0xffff0000, v72
	v_and_b32_e32 v83, 0xffff0000, v73
	v_fmac_f32_e32 v68, v74, v74
	v_lshlrev_b32_e32 v80, 16, v72
	v_lshlrev_b32_e32 v82, 16, v73
	v_add_f32_e32 v68, v69, v68
	v_mul_f32_e32 v69, v81, v81
	v_mul_f32_e32 v74, v83, v83
	v_fmac_f32_e32 v69, v80, v80
	v_fmac_f32_e32 v74, v82, v82
	v_add_f32_e32 v69, v69, v74
	v_add_f32_e32 v68, v68, v69
	v_add_f32_e32 v68, v88, v68
	ds_bpermute_b32 v69, v237, v68
	v_lshl_add_u64 v[74:75], s[14:15], 0, v[222:223]
	v_lshl_add_u64 v[74:75], v[214:215], 1, v[74:75]
	global_store_dwordx4 v[74:75], v[76:79], off nt
	global_store_dwordx4 v[74:75], v[70:73], off offset:256 nt
	s_waitcnt lgkmcnt(0)
	v_add_f32_e32 v68, v68, v69
	ds_bpermute_b32 v69, v238, v68
	s_and_saveexec_b64 s[4:5], vcc
	s_cbranch_execz .LBB0_1129
	v_lshlrev_b64 v[70:71], 6, v[220:221]
	v_lshl_add_u64 v[70:71], s[18:19], 0, v[70:71]
	v_lshl_add_u64 v[70:71], s[44:45], 2, v[70:71]
	s_lshl_b32 s56, s53, 2
	v_lshl_add_u64 v[70:71], v[70:71], 0, s[56:57]
	s_waitcnt lgkmcnt(0)
	v_add_f32_e32 v68, v68, v69
	global_store_dword v[70:71], v68, off
.LBB0_1129:
	s_or_b64 exec, exec, s[4:5]
	v_lshlrev_b32_e32 v68, 16, v160
	s_waitcnt lgkmcnt(0)
	v_and_b32_e32 v69, 0xffff0000, v160
	v_lshlrev_b32_e32 v70, 16, v161
	v_and_b32_e32 v71, 0xffff0000, v161
	v_lshlrev_b32_e32 v72, 16, v162
	v_and_b32_e32 v73, 0xffff0000, v162
	v_lshlrev_b32_e32 v74, 16, v163
	v_and_b32_e32 v75, 0xffff0000, v163
	v_pk_add_f32 v[64:65], v[64:65], v[68:69]
	v_pk_add_f32 v[66:67], v[66:67], v[70:71]
	v_pk_add_f32 v[68:69], v[62:63], v[74:75]
	v_pk_add_f32 v[62:63], v[60:61], v[72:73]
	v_cvt_pk_bf16_f32 v60, v64, v65
	v_cvt_pk_bf16_f32 v61, v66, v67
	v_and_b32_e32 v65, 0xffff0000, v60
	v_lshlrev_b32_e32 v64, 16, v60
	v_and_b32_e32 v67, 0xffff0000, v61
	v_mul_f32_e32 v65, v65, v65
	v_cvt_pk_bf16_f32 v62, v62, v63
	v_cvt_pk_bf16_f32 v63, v68, v69
	v_lshlrev_b32_e32 v66, 16, v61
	v_fmac_f32_e32 v65, v64, v64
	v_mul_f32_e32 v64, v67, v67
	v_and_b32_e32 v69, 0xffff0000, v62
	v_and_b32_e32 v71, 0xffff0000, v63
	v_fmac_f32_e32 v64, v66, v66
	v_lshlrev_b32_e32 v68, 16, v62
	v_lshlrev_b32_e32 v70, 16, v63
	v_add_f32_e32 v64, v65, v64
	v_mul_f32_e32 v65, v69, v69
	v_mul_f32_e32 v66, v71, v71
	v_fmac_f32_e32 v65, v68, v68
	v_fmac_f32_e32 v66, v70, v70
	v_add_f32_e32 v65, v65, v66
	v_add_f32_e32 v72, v64, v65
	v_lshlrev_b32_e32 v64, 16, v156
	v_and_b32_e32 v65, 0xffff0000, v156
	v_lshlrev_b32_e32 v66, 16, v157
	v_and_b32_e32 v67, 0xffff0000, v157
	v_lshlrev_b32_e32 v68, 16, v158
	v_and_b32_e32 v69, 0xffff0000, v158
	v_lshlrev_b32_e32 v70, 16, v159
	v_and_b32_e32 v71, 0xffff0000, v159
	v_pk_add_f32 v[56:57], v[56:57], v[64:65]
	v_pk_add_f32 v[58:59], v[58:59], v[66:67]
	v_pk_add_f32 v[64:65], v[54:55], v[70:71]
	v_pk_add_f32 v[52:53], v[52:53], v[68:69]
	v_cvt_pk_bf16_f32 v54, v56, v57
	v_cvt_pk_bf16_f32 v55, v58, v59
	v_cvt_pk_bf16_f32 v56, v52, v53
	v_and_b32_e32 v53, 0xffff0000, v54
	v_lshlrev_b32_e32 v52, 16, v54
	v_and_b32_e32 v59, 0xffff0000, v55
	v_mul_f32_e32 v53, v53, v53
	v_cvt_pk_bf16_f32 v57, v64, v65
	v_lshlrev_b32_e32 v58, 16, v55
	v_fmac_f32_e32 v53, v52, v52
	v_mul_f32_e32 v52, v59, v59
	v_and_b32_e32 v65, 0xffff0000, v56
	v_and_b32_e32 v67, 0xffff0000, v57
	v_fmac_f32_e32 v52, v58, v58
	v_lshlrev_b32_e32 v64, 16, v56
	v_lshlrev_b32_e32 v66, 16, v57
	v_add_f32_e32 v52, v53, v52
	v_mul_f32_e32 v53, v65, v65
	v_mul_f32_e32 v58, v67, v67
	v_fmac_f32_e32 v53, v64, v64
	v_fmac_f32_e32 v58, v66, v66
	v_add_f32_e32 v53, v53, v58
	v_add_f32_e32 v52, v52, v53
	v_add_f32_e32 v52, v72, v52
	ds_bpermute_b32 v53, v237, v52
	v_lshlrev_b64 v[58:59], 10, v[218:219]
	v_lshl_add_u64 v[58:59], v[58:59], 1, s[14:15]
	v_lshl_add_u64 v[58:59], v[214:215], 1, v[58:59]
	global_store_dwordx4 v[58:59], v[60:63], off nt
	global_store_dwordx4 v[58:59], v[54:57], off offset:256 nt
	s_waitcnt lgkmcnt(0)
	v_add_f32_e32 v52, v52, v53
	ds_bpermute_b32 v53, v238, v52
	s_and_saveexec_b64 s[4:5], vcc
	s_cbranch_execz .LBB0_1131
	v_lshlrev_b64 v[54:55], 6, v[218:219]
	v_lshl_add_u64 v[54:55], s[18:19], 0, v[54:55]
	v_lshl_add_u64 v[54:55], s[44:45], 2, v[54:55]
	s_lshl_b32 s56, s53, 2
	v_lshl_add_u64 v[54:55], v[54:55], 0, s[56:57]
	s_waitcnt lgkmcnt(0)
	v_add_f32_e32 v52, v52, v53
	global_store_dword v[54:55], v52, off
.LBB0_1131:
	s_or_b64 exec, exec, s[4:5]
	v_lshlrev_b32_e32 v52, 16, v152
	s_waitcnt lgkmcnt(0)
	v_and_b32_e32 v53, 0xffff0000, v152
	v_lshlrev_b32_e32 v54, 16, v153
	v_and_b32_e32 v55, 0xffff0000, v153
	v_lshlrev_b32_e32 v56, 16, v154
	v_and_b32_e32 v57, 0xffff0000, v154
	v_lshlrev_b32_e32 v58, 16, v155
	v_and_b32_e32 v59, 0xffff0000, v155
	v_pk_add_f32 v[48:49], v[48:49], v[52:53]
	v_pk_add_f32 v[50:51], v[50:51], v[54:55]
	v_pk_add_f32 v[52:53], v[46:47], v[58:59]
	v_pk_add_f32 v[46:47], v[44:45], v[56:57]
	v_cvt_pk_bf16_f32 v44, v48, v49
	v_cvt_pk_bf16_f32 v45, v50, v51
	v_and_b32_e32 v49, 0xffff0000, v44
	v_lshlrev_b32_e32 v48, 16, v44
	v_and_b32_e32 v51, 0xffff0000, v45
	v_mul_f32_e32 v49, v49, v49
	v_cvt_pk_bf16_f32 v46, v46, v47
	v_cvt_pk_bf16_f32 v47, v52, v53
	v_lshlrev_b32_e32 v50, 16, v45
	v_fmac_f32_e32 v49, v48, v48
	v_mul_f32_e32 v48, v51, v51
	v_and_b32_e32 v53, 0xffff0000, v46
	v_and_b32_e32 v55, 0xffff0000, v47
	v_fmac_f32_e32 v48, v50, v50
	v_lshlrev_b32_e32 v52, 16, v46
	v_lshlrev_b32_e32 v54, 16, v47
	v_add_f32_e32 v48, v49, v48
	v_mul_f32_e32 v49, v53, v53
	v_mul_f32_e32 v50, v55, v55
	v_fmac_f32_e32 v49, v52, v52
	v_fmac_f32_e32 v50, v54, v54
	v_add_f32_e32 v49, v49, v50
	v_add_f32_e32 v56, v48, v49
	v_lshlrev_b32_e32 v48, 16, v148
	v_and_b32_e32 v49, 0xffff0000, v148
	v_lshlrev_b32_e32 v50, 16, v149
	v_and_b32_e32 v51, 0xffff0000, v149
	v_lshlrev_b32_e32 v52, 16, v150
	v_and_b32_e32 v53, 0xffff0000, v150
	v_pk_add_f32 v[40:41], v[40:41], v[48:49]
	v_lshlrev_b32_e32 v54, 16, v151
	v_and_b32_e32 v55, 0xffff0000, v151
	v_pk_add_f32 v[42:43], v[42:43], v[50:51]
	v_pk_add_f32 v[36:37], v[36:37], v[52:53]
	v_cvt_pk_bf16_f32 v40, v40, v41
	v_pk_add_f32 v[38:39], v[38:39], v[54:55]
	v_cvt_pk_bf16_f32 v41, v42, v43
	v_cvt_pk_bf16_f32 v42, v36, v37
	v_and_b32_e32 v37, 0xffff0000, v40
	v_cvt_pk_bf16_f32 v43, v38, v39
	v_lshlrev_b32_e32 v36, 16, v40
	v_and_b32_e32 v39, 0xffff0000, v41
	v_mul_f32_e32 v37, v37, v37
	v_lshlrev_b32_e32 v38, 16, v41
	v_fmac_f32_e32 v37, v36, v36
	v_mul_f32_e32 v36, v39, v39
	v_and_b32_e32 v49, 0xffff0000, v42
	v_and_b32_e32 v51, 0xffff0000, v43
	v_fmac_f32_e32 v36, v38, v38
	v_lshlrev_b32_e32 v48, 16, v42
	v_lshlrev_b32_e32 v50, 16, v43
	v_add_f32_e32 v36, v37, v36
	v_mul_f32_e32 v37, v49, v49
	v_mul_f32_e32 v38, v51, v51
	v_fmac_f32_e32 v37, v48, v48
	v_fmac_f32_e32 v38, v50, v50
	v_add_f32_e32 v37, v37, v38
	v_add_f32_e32 v36, v36, v37
	v_add_f32_e32 v38, v56, v36
	ds_bpermute_b32 v39, v237, v38
	v_add_u32_e32 v36, 0x90, v216
	v_ashrrev_i32_e32 v37, 31, v36
	v_lshlrev_b64 v[48:49], 11, v[36:37]
	v_lshl_add_u64 v[48:49], s[14:15], 0, v[48:49]
	s_waitcnt lgkmcnt(0)
	v_add_f32_e32 v38, v38, v39
	ds_bpermute_b32 v39, v238, v38
	v_lshl_add_u64 v[48:49], v[214:215], 1, v[48:49]
	global_store_dwordx4 v[48:49], v[44:47], off nt
	global_store_dwordx4 v[48:49], v[40:43], off offset:256 nt
	s_and_saveexec_b64 s[4:5], vcc
	s_cbranch_execz .LBB0_1133
	v_lshlrev_b64 v[36:37], 6, v[36:37]
	v_lshl_add_u64 v[36:37], s[18:19], 0, v[36:37]
	v_lshl_add_u64 v[36:37], s[44:45], 2, v[36:37]
	s_lshl_b32 s56, s53, 2
	v_lshl_add_u64 v[36:37], v[36:37], 0, s[56:57]
	s_waitcnt lgkmcnt(0)
	v_add_f32_e32 v38, v38, v39
	global_store_dword v[36:37], v38, off
.LBB0_1133:
	s_or_b64 exec, exec, s[4:5]
	v_lshlrev_b32_e32 v36, 16, v136
	v_and_b32_e32 v37, 0xffff0000, v136
	v_lshlrev_b32_e32 v38, 16, v137
	s_waitcnt lgkmcnt(0)
	v_and_b32_e32 v39, 0xffff0000, v137
	v_lshlrev_b32_e32 v40, 16, v138
	v_and_b32_e32 v41, 0xffff0000, v138
	v_lshlrev_b32_e32 v42, 16, v139
	v_and_b32_e32 v43, 0xffff0000, v139
	v_pk_add_f32 v[32:33], v[32:33], v[36:37]
	v_pk_add_f32 v[34:35], v[34:35], v[38:39]
	v_pk_add_f32 v[36:37], v[30:31], v[42:43]
	v_pk_add_f32 v[30:31], v[28:29], v[40:41]
	v_cvt_pk_bf16_f32 v28, v32, v33
	v_cvt_pk_bf16_f32 v29, v34, v35
	v_and_b32_e32 v33, 0xffff0000, v28
	v_lshlrev_b32_e32 v32, 16, v28
	v_and_b32_e32 v35, 0xffff0000, v29
	v_mul_f32_e32 v33, v33, v33
	v_cvt_pk_bf16_f32 v30, v30, v31
	v_cvt_pk_bf16_f32 v31, v36, v37
	v_lshlrev_b32_e32 v34, 16, v29
	v_fmac_f32_e32 v33, v32, v32
	v_mul_f32_e32 v32, v35, v35
	v_and_b32_e32 v37, 0xffff0000, v30
	v_and_b32_e32 v39, 0xffff0000, v31
	v_fmac_f32_e32 v32, v34, v34
	v_lshlrev_b32_e32 v36, 16, v30
	v_lshlrev_b32_e32 v38, 16, v31
	v_add_f32_e32 v32, v33, v32
	v_mul_f32_e32 v33, v37, v37
	v_mul_f32_e32 v34, v39, v39
	v_fmac_f32_e32 v33, v36, v36
	v_fmac_f32_e32 v34, v38, v38
	v_add_f32_e32 v33, v33, v34
	v_add_f32_e32 v40, v32, v33
	v_lshlrev_b32_e32 v32, 16, v128
	v_and_b32_e32 v33, 0xffff0000, v128
	v_lshlrev_b32_e32 v34, 16, v129
	v_and_b32_e32 v35, 0xffff0000, v129
	v_lshlrev_b32_e32 v36, 16, v130
	v_and_b32_e32 v37, 0xffff0000, v130
	v_pk_add_f32 v[24:25], v[24:25], v[32:33]
	v_lshlrev_b32_e32 v38, 16, v131
	v_and_b32_e32 v39, 0xffff0000, v131
	v_pk_add_f32 v[26:27], v[26:27], v[34:35]
	v_pk_add_f32 v[20:21], v[20:21], v[36:37]
	v_cvt_pk_bf16_f32 v24, v24, v25
	v_pk_add_f32 v[22:23], v[22:23], v[38:39]
	v_cvt_pk_bf16_f32 v25, v26, v27
	v_cvt_pk_bf16_f32 v26, v20, v21
	v_and_b32_e32 v21, 0xffff0000, v24
	v_cvt_pk_bf16_f32 v27, v22, v23
	v_lshlrev_b32_e32 v20, 16, v24
	v_and_b32_e32 v23, 0xffff0000, v25
	v_mul_f32_e32 v21, v21, v21
	v_lshlrev_b32_e32 v22, 16, v25
	v_fmac_f32_e32 v21, v20, v20
	v_mul_f32_e32 v20, v23, v23
	v_and_b32_e32 v33, 0xffff0000, v26
	v_and_b32_e32 v35, 0xffff0000, v27
	v_fmac_f32_e32 v20, v22, v22
	v_lshlrev_b32_e32 v32, 16, v26
	v_lshlrev_b32_e32 v34, 16, v27
	v_add_f32_e32 v20, v21, v20
	v_mul_f32_e32 v21, v33, v33
	v_mul_f32_e32 v22, v35, v35
	v_fmac_f32_e32 v21, v32, v32
	v_fmac_f32_e32 v22, v34, v34
	v_add_f32_e32 v21, v21, v22
	v_add_f32_e32 v20, v20, v21
	v_add_f32_e32 v22, v40, v20
	ds_bpermute_b32 v23, v237, v22
	v_add_u32_e32 v20, 0xa0, v216
	v_ashrrev_i32_e32 v21, 31, v20
	v_lshlrev_b64 v[32:33], 11, v[20:21]
	v_lshl_add_u64 v[32:33], s[14:15], 0, v[32:33]
	s_waitcnt lgkmcnt(0)
	v_add_f32_e32 v22, v22, v23
	ds_bpermute_b32 v23, v238, v22
	v_lshl_add_u64 v[32:33], v[214:215], 1, v[32:33]
	global_store_dwordx4 v[32:33], v[28:31], off nt
	global_store_dwordx4 v[32:33], v[24:27], off offset:256 nt
	s_and_saveexec_b64 s[4:5], vcc
	s_cbranch_execz .LBB0_1135
	v_lshlrev_b64 v[20:21], 6, v[20:21]
	v_lshl_add_u64 v[20:21], s[18:19], 0, v[20:21]
	v_lshl_add_u64 v[20:21], s[44:45], 2, v[20:21]
	s_lshl_b32 s56, s53, 2
	v_lshl_add_u64 v[20:21], v[20:21], 0, s[56:57]
	s_waitcnt lgkmcnt(0)
	v_add_f32_e32 v22, v22, v23
	global_store_dword v[20:21], v22, off
.LBB0_1135:
	s_or_b64 exec, exec, s[4:5]
	v_lshlrev_b32_e32 v20, 16, v116
	v_and_b32_e32 v21, 0xffff0000, v116
	v_lshlrev_b32_e32 v22, 16, v117
	s_waitcnt lgkmcnt(0)
	v_and_b32_e32 v23, 0xffff0000, v117
	v_lshlrev_b32_e32 v24, 16, v118
	v_and_b32_e32 v25, 0xffff0000, v118
	v_lshlrev_b32_e32 v26, 16, v119
	v_and_b32_e32 v27, 0xffff0000, v119
	v_pk_add_f32 v[16:17], v[16:17], v[20:21]
	v_pk_add_f32 v[18:19], v[18:19], v[22:23]
	v_pk_add_f32 v[20:21], v[14:15], v[26:27]
	v_pk_add_f32 v[14:15], v[12:13], v[24:25]
	v_cvt_pk_bf16_f32 v12, v16, v17
	v_cvt_pk_bf16_f32 v13, v18, v19
	v_and_b32_e32 v17, 0xffff0000, v12
	v_lshlrev_b32_e32 v16, 16, v12
	v_and_b32_e32 v19, 0xffff0000, v13
	v_mul_f32_e32 v17, v17, v17
	v_cvt_pk_bf16_f32 v14, v14, v15
	v_cvt_pk_bf16_f32 v15, v20, v21
	v_lshlrev_b32_e32 v18, 16, v13
	v_fmac_f32_e32 v17, v16, v16
	v_mul_f32_e32 v16, v19, v19
	v_and_b32_e32 v21, 0xffff0000, v14
	v_and_b32_e32 v23, 0xffff0000, v15
	v_fmac_f32_e32 v16, v18, v18
	v_lshlrev_b32_e32 v20, 16, v14
	v_lshlrev_b32_e32 v22, 16, v15
	v_add_f32_e32 v16, v17, v16
	v_mul_f32_e32 v17, v21, v21
	v_mul_f32_e32 v18, v23, v23
	v_fmac_f32_e32 v17, v20, v20
	v_fmac_f32_e32 v18, v22, v22
	v_add_f32_e32 v17, v17, v18
	v_add_f32_e32 v24, v16, v17
	v_lshlrev_b32_e32 v16, 16, v108
	v_and_b32_e32 v17, 0xffff0000, v108
	v_lshlrev_b32_e32 v18, 16, v109
	v_and_b32_e32 v19, 0xffff0000, v109
	v_lshlrev_b32_e32 v20, 16, v110
	v_and_b32_e32 v21, 0xffff0000, v110
	v_pk_add_f32 v[8:9], v[8:9], v[16:17]
	v_lshlrev_b32_e32 v22, 16, v111
	v_and_b32_e32 v23, 0xffff0000, v111
	v_pk_add_f32 v[10:11], v[10:11], v[18:19]
	v_pk_add_f32 v[4:5], v[4:5], v[20:21]
	v_cvt_pk_bf16_f32 v8, v8, v9
	v_pk_add_f32 v[6:7], v[6:7], v[22:23]
	v_cvt_pk_bf16_f32 v9, v10, v11
	v_cvt_pk_bf16_f32 v10, v4, v5
	v_and_b32_e32 v5, 0xffff0000, v8
	v_cvt_pk_bf16_f32 v11, v6, v7
	v_lshlrev_b32_e32 v4, 16, v8
	v_and_b32_e32 v7, 0xffff0000, v9
	v_mul_f32_e32 v5, v5, v5
	v_lshlrev_b32_e32 v6, 16, v9
	v_fmac_f32_e32 v5, v4, v4
	v_mul_f32_e32 v4, v7, v7
	v_and_b32_e32 v17, 0xffff0000, v10
	v_and_b32_e32 v19, 0xffff0000, v11
	v_fmac_f32_e32 v4, v6, v6
	v_lshlrev_b32_e32 v16, 16, v10
	v_lshlrev_b32_e32 v18, 16, v11
	v_add_f32_e32 v4, v5, v4
	v_mul_f32_e32 v5, v17, v17
	v_mul_f32_e32 v6, v19, v19
	v_fmac_f32_e32 v5, v16, v16
	v_fmac_f32_e32 v6, v18, v18
	v_add_f32_e32 v5, v5, v6
	v_add_f32_e32 v4, v4, v5
	v_add_f32_e32 v6, v24, v4
	ds_bpermute_b32 v7, v237, v6
	v_add_u32_e32 v4, 0xb0, v216
	v_ashrrev_i32_e32 v5, 31, v4
	v_lshlrev_b64 v[16:17], 11, v[4:5]
	v_lshl_add_u64 v[16:17], s[14:15], 0, v[16:17]
	s_waitcnt lgkmcnt(0)
	v_add_f32_e32 v6, v6, v7
	ds_bpermute_b32 v7, v238, v6
	v_lshl_add_u64 v[16:17], v[214:215], 1, v[16:17]
	global_store_dwordx4 v[16:17], v[12:15], off nt
	global_store_dwordx4 v[16:17], v[8:11], off offset:256 nt
	s_and_saveexec_b64 s[4:5], vcc
	s_cbranch_execz .LBB0_1137
	v_lshlrev_b64 v[4:5], 6, v[4:5]
	v_lshl_add_u64 v[4:5], s[18:19], 0, v[4:5]
	v_lshl_add_u64 v[4:5], s[44:45], 2, v[4:5]
	s_lshl_b32 s56, s53, 2
	v_lshl_add_u64 v[4:5], v[4:5], 0, s[56:57]
	s_waitcnt lgkmcnt(0)
	v_add_f32_e32 v6, v6, v7
	global_store_dword v[4:5], v6, off

.LBB0_1209:
	s_lshl_b32 s4, s60, 8
	v_mov_b32_e32 v152, v0
	s_add_i32 s4, s4, s51
	v_cvt_pk_bf16_f32 v72, v72, v73
	v_and_or_b32 v142, v152, 15, s4
	s_lshl_b32 s4, s59, 8
	v_lshrrev_b32_e32 v152, 1, v152
	s_or_b32 s4, s4, s52
	v_ashrrev_i32_e32 v143, 31, v142
	v_and_or_b32 v152, v152, 24, s4
	v_or_b32_e32 v144, 16, v142
	v_or_b32_e32 v148, 32, v142
	v_or_b32_e32 v150, 48, v142
	v_ashrrev_i32_e32 v153, 31, v152
	v_lshlrev_b64 v[142:143], 11, v[142:143]
	v_lshl_add_u64 v[142:143], s[14:15], 0, v[142:143]
	v_lshlrev_b64 v[152:153], 1, v[152:153]
	v_lshl_add_u64 v[142:143], v[142:143], 0, v[152:153]
	s_mov_b64 s[4:5], 0x40000
	v_cvt_pk_bf16_f32 v73, v74, v75
	v_cvt_pk_bf16_f32 v74, v68, v69
	v_lshl_add_u64 v[68:69], v[142:143], 0, s[4:5]
	s_mov_b32 s4, 0x40000
	v_cvt_pk_bf16_f32 v64, v64, v65
	v_cvt_pk_bf16_f32 v65, v66, v67
	v_cvt_pk_bf16_f32 v66, v60, v61
	v_add_co_u32_e32 v60, vcc, s4, v142
	v_cvt_pk_bf16_f32 v48, v48, v49
	v_cvt_pk_bf16_f32 v49, v50, v51
	v_cvt_pk_bf16_f32 v50, v44, v45
	v_cvt_pk_bf16_f32 v51, v46, v47
	s_mov_b64 s[4:5], 0x48000
	v_addc_co_u32_e32 v61, vcc, 0, v143, vcc
	global_store_dwordx4 v[68:69], v[48:51], off offset:256 nt
	v_cvt_pk_bf16_f32 v32, v32, v33
	v_cvt_pk_bf16_f32 v33, v34, v35
	v_lshl_add_u64 v[48:49], v[142:143], 0, s[4:5]
	s_mov_b32 s4, 0x48000
	v_add_co_u32_e32 v50, vcc, s4, v142
	v_cvt_pk_bf16_f32 v34, v28, v29
	v_cvt_pk_bf16_f32 v35, v30, v31
	s_mov_b64 s[4:5], 0x50000
	v_ashrrev_i32_e32 v145, 31, v144
	v_addc_co_u32_e32 v51, vcc, 0, v143, vcc
	global_store_dwordx4 v[48:49], v[32:35], off offset:256 nt
	v_ashrrev_i32_e32 v149, 31, v148
	v_cvt_pk_bf16_f32 v112, v112, v113
	v_lshl_add_u64 v[32:33], v[142:143], 0, s[4:5]
	s_mov_b32 s4, 0x50000
	v_cvt_pk_bf16_f32 v113, v114, v115
	v_cvt_pk_bf16_f32 v114, v108, v109
	v_lshlrev_b64 v[108:109], 11, v[144:145]
	v_add_co_u32_e32 v34, vcc, s4, v142
	v_cvt_pk_bf16_f32 v16, v16, v17
	v_cvt_pk_bf16_f32 v17, v18, v19
	v_cvt_pk_bf16_f32 v18, v12, v13
	v_cvt_pk_bf16_f32 v19, v14, v15
	s_mov_b64 s[4:5], 0x58000
	v_ashrrev_i32_e32 v151, 31, v150
	v_cvt_pk_bf16_f32 v115, v110, v111
	v_lshl_add_u64 v[108:109], s[14:15], 0, v[108:109]
	v_cvt_pk_bf16_f32 v96, v96, v97
	v_cvt_pk_bf16_f32 v97, v98, v99
	v_cvt_pk_bf16_f32 v98, v92, v93
	v_lshlrev_b64 v[92:93], 11, v[148:149]
	v_addc_co_u32_e32 v35, vcc, 0, v143, vcc
	global_store_dwordx4 v[32:33], v[16:19], off offset:256 nt
	global_store_dwordx4 v[142:143], v[112:115], off offset:256 nt
	v_cvt_pk_bf16_f32 v99, v94, v95
	v_lshl_add_u64 v[16:17], v[142:143], 0, s[4:5]
	s_mov_b32 s4, 0x58000
	v_lshl_add_u64 v[112:113], v[108:109], 0, v[152:153]
	v_lshl_add_u64 v[92:93], s[14:15], 0, v[92:93]
	v_cvt_pk_bf16_f32 v80, v80, v81
	v_cvt_pk_bf16_f32 v81, v82, v83
	v_cvt_pk_bf16_f32 v82, v76, v77
	v_lshlrev_b64 v[76:77], 11, v[150:151]
	v_add_co_u32_e32 v18, vcc, s4, v142
	global_store_dwordx4 v[112:113], v[96:99], off offset:256 nt
	v_cvt_pk_bf16_f32 v83, v78, v79
	v_lshl_add_u64 v[76:77], s[14:15], 0, v[76:77]
	v_lshl_add_u64 v[96:97], v[92:93], 0, v[152:153]
	v_addc_co_u32_e32 v19, vcc, 0, v143, vcc
	v_cvt_pk_bf16_f32 v128, v128, v129
	v_cvt_pk_bf16_f32 v129, v130, v131
	v_cvt_pk_bf16_f32 v130, v124, v125
	v_cvt_pk_bf16_f32 v131, v126, v127
	v_cvt_pk_bf16_f32 v108, v120, v121
	v_cvt_pk_bf16_f32 v109, v122, v123
	v_cvt_pk_bf16_f32 v110, v116, v117
	v_cvt_pk_bf16_f32 v111, v118, v119
	v_cvt_pk_bf16_f32 v92, v104, v105
	v_cvt_pk_bf16_f32 v93, v106, v107
	v_cvt_pk_bf16_f32 v94, v100, v101
	v_cvt_pk_bf16_f32 v95, v102, v103
	global_store_dwordx4 v[96:97], v[80:83], off offset:256 nt
	v_cvt_pk_bf16_f32 v78, v84, v85
	v_cvt_pk_bf16_f32 v79, v86, v87
	v_lshl_add_u64 v[80:81], v[76:77], 0, v[152:153]
	v_cvt_pk_bf16_f32 v76, v88, v89
	v_cvt_pk_bf16_f32 v77, v90, v91
	v_cvt_pk_bf16_f32 v75, v70, v71
	v_cvt_pk_bf16_f32 v67, v62, v63
	v_cvt_pk_bf16_f32 v44, v56, v57
	v_cvt_pk_bf16_f32 v45, v58, v59
	v_cvt_pk_bf16_f32 v46, v52, v53
	v_cvt_pk_bf16_f32 v47, v54, v55
	v_cvt_pk_bf16_f32 v28, v40, v41
	v_cvt_pk_bf16_f32 v29, v42, v43
	v_cvt_pk_bf16_f32 v30, v36, v37
	v_cvt_pk_bf16_f32 v31, v38, v39
	v_cvt_pk_bf16_f32 v12, v24, v25
	v_cvt_pk_bf16_f32 v13, v26, v27
	v_cvt_pk_bf16_f32 v14, v20, v21
	v_cvt_pk_bf16_f32 v15, v22, v23
	v_cvt_pk_bf16_f32 v8, v8, v9
	v_cvt_pk_bf16_f32 v9, v10, v11
	v_cvt_pk_bf16_f32 v10, v4, v5
	v_cvt_pk_bf16_f32 v11, v6, v7
	s_andn2_b64 vcc, exec, s[38:39]
	s_mov_b64 s[4:5], -1
	global_store_dwordx4 v[142:143], v[128:131], off nt
	global_store_dwordx4 v[112:113], v[108:111], off nt
	global_store_dwordx4 v[96:97], v[92:95], off nt
	global_store_dwordx4 v[80:81], v[76:79], off nt
	global_store_dwordx4 v[80:81], v[72:75], off offset:256 nt
	global_store_dwordx4 v[60:61], v[64:67], off nt
	global_store_dwordx4 v[50:51], v[44:47], off nt
	global_store_dwordx4 v[34:35], v[28:31], off nt
	global_store_dwordx4 v[18:19], v[12:15], off nt
	global_store_dwordx4 v[16:17], v[8:11], off offset:256 nt
	s_cbranch_vccnz .LBB0_1198
	s_andn2_b64 vcc, exec, s[10:11]
	s_cbranch_vccnz .LBB0_1197
	s_barrier
	s_branch .LBB0_1197

.LBB0_1462:
	s_lshl_b32 s4, s65, 8
	v_mov_b32_e32 v112, v0
	s_add_i32 s4, s4, s60
	v_and_b32_e32 v198, 64, v250
	v_and_or_b32 v216, v112, 15, s4
	v_ashrrev_i32_e32 v217, 31, v216
	v_bfe_u32 v196, v112, 4, 2
	v_lshl_add_u64 v[112:113], v[216:217], 2, s[20:21]
	global_load_dword v114, v[112:113], off
	global_load_dword v243, v[112:113], off offset:512
	v_or_b32_e32 v226, 16, v216
	v_ashrrev_i32_e32 v227, 31, v226
	v_or_b32_e32 v222, 32, v216
	v_ashrrev_i32_e32 v223, 31, v222
	v_or_b32_e32 v220, 48, v216
	v_ashrrev_i32_e32 v221, 31, v220
	v_add_u32_e32 v112, 0x90, v216
	v_ashrrev_i32_e32 v113, 31, v112
	s_lshl_b32 s4, s56, 8
	s_or_b32 s4, s4, s61
	v_lshl_or_b32 v214, v196, 3, s4
	v_ashrrev_i32_e32 v215, 31, v214
	v_lshlrev_b64 v[234:235], 1, v[214:215]
	v_lshlrev_b64 v[236:237], 11, v[216:217]
	v_lshlrev_b64 v[230:231], 11, v[226:227]
	v_lshlrev_b64 v[228:229], 11, v[222:223]
	v_add_u32_e32 v218, 0x80, v216
	v_lshlrev_b64 v[224:225], 11, v[220:221]
	v_ashrrev_i32_e32 v219, 31, v218
	v_xor_b32_e32 v197, 16, v250
	v_add_u32_e32 v198, 64, v198
	v_cmp_lt_i32_e32 vcc, v197, v198
	s_lshl_b32 s48, s56, 2
	s_ashr_i32 s49, s48, 31
	v_cndmask_b32_e32 v197, v250, v197, vcc
	v_lshlrev_b32_e32 v240, 2, v197
	v_xor_b32_e32 v197, 32, v250
	v_cmp_lt_i32_e32 vcc, v197, v198
	s_waitcnt vmcnt(0)
	v_mul_f32_e32 v232, v114, v114
	v_lshl_add_u64 v[114:115], v[226:227], 2, s[20:21]
	global_load_dword v246, v[114:115], off
	v_lshl_add_u64 v[114:115], v[222:223], 2, s[20:21]
	global_load_dword v245, v[114:115], off
	v_lshl_add_u64 v[114:115], v[220:221], 2, s[20:21]
	global_load_dword v244, v[114:115], off
	v_lshl_add_u64 v[114:115], v[112:113], 2, s[20:21]
	global_load_dword v242, v[114:115], off
	v_add_u32_e32 v114, 0xa0, v216
	v_ashrrev_i32_e32 v115, 31, v114
	v_lshl_add_u64 v[120:121], v[114:115], 2, s[20:21]
	global_load_dword v239, v[120:121], off
	v_add_u32_e32 v120, 0xb0, v216
	v_ashrrev_i32_e32 v121, 31, v120
	v_lshl_add_u64 v[122:123], v[120:121], 2, s[20:21]
	global_load_dword v238, v[122:123], off
	v_lshl_add_u64 v[122:123], s[14:15], 0, v[234:235]
	v_lshl_add_u64 v[132:133], v[122:123], 0, v[236:237]
	global_load_dwordx4 v[192:195], v[132:133], off
	global_load_dwordx4 v[188:191], v[132:133], off offset:256
	v_lshl_add_u64 v[132:133], v[122:123], 0, v[230:231]
	global_load_dwordx4 v[184:187], v[132:133], off
	global_load_dwordx4 v[180:183], v[132:133], off offset:256
	v_lshl_add_u64 v[132:133], v[122:123], 0, v[228:229]
	global_load_dwordx4 v[176:179], v[132:133], off
	global_load_dwordx4 v[172:175], v[132:133], off offset:256
	v_lshl_add_u64 v[132:133], v[122:123], 0, v[224:225]
	global_load_dwordx4 v[168:171], v[132:133], off
	global_load_dwordx4 v[164:167], v[132:133], off offset:256
	v_lshlrev_b64 v[132:133], 11, v[218:219]
	v_lshlrev_b64 v[112:113], 11, v[112:113]
	v_lshl_add_u64 v[132:133], v[122:123], 0, v[132:133]
	v_lshl_add_u64 v[112:113], v[122:123], 0, v[112:113]
	global_load_dwordx4 v[160:163], v[132:133], off
	global_load_dwordx4 v[156:159], v[132:133], off offset:256
	global_load_dwordx4 v[152:155], v[112:113], off
	global_load_dwordx4 v[148:151], v[112:113], off offset:256
	v_lshlrev_b64 v[112:113], 11, v[114:115]
	v_lshl_add_u64 v[112:113], v[122:123], 0, v[112:113]
	global_load_dwordx4 v[144:147], v[112:113], off
	global_load_dwordx4 v[132:135], v[112:113], off offset:256
	v_lshlrev_b64 v[112:113], 11, v[120:121]
	v_lshl_add_u64 v[112:113], v[122:123], 0, v[112:113]
	global_load_dwordx4 v[120:123], v[112:113], off
	s_nop 0
	global_load_dwordx4 v[112:115], v[112:113], off offset:256
	v_cndmask_b32_e32 v197, v250, v197, vcc
	v_lshlrev_b32_e32 v241, 2, v197
	v_cmp_eq_u32_e32 vcc, 0, v196
	s_waitcnt vmcnt(15)
	v_lshlrev_b32_e32 v196, 16, v192
	v_and_b32_e32 v197, 0xffff0000, v192
	v_lshlrev_b32_e32 v192, 16, v193
	v_and_b32_e32 v193, 0xffff0000, v193
	v_lshlrev_b32_e32 v198, 16, v194
	v_and_b32_e32 v199, 0xffff0000, v194
	v_lshlrev_b32_e32 v194, 16, v195
	v_and_b32_e32 v195, 0xffff0000, v195
	v_pk_fma_f32 v[140:141], v[140:141], v[232:233], v[196:197] op_sel_hi:[1,0,1]
	v_pk_fma_f32 v[142:143], v[142:143], v[232:233], v[192:193] op_sel_hi:[1,0,1]
	v_pk_fma_f32 v[192:193], v[138:139], v[232:233], v[194:195] op_sel_hi:[1,0,1]
	v_pk_fma_f32 v[138:139], v[136:137], v[232:233], v[198:199] op_sel_hi:[1,0,1]
	v_cvt_pk_bf16_f32 v136, v140, v141
	v_lshl_add_u64 v[140:141], s[14:15], 0, v[236:237]
	v_cvt_pk_bf16_f32 v137, v142, v143
	v_cvt_pk_bf16_f32 v138, v138, v139
	v_cvt_pk_bf16_f32 v139, v192, v193
	v_lshl_add_u64 v[140:141], v[140:141], 0, v[234:235]
	global_store_dwordx4 v[140:141], v[136:139], off nt
	v_lshlrev_b32_e32 v142, 16, v136
	v_lshlrev_b32_e32 v143, 16, v137
	v_and_b32_e32 v136, 0xffff0000, v136
	v_and_b32_e32 v137, 0xffff0000, v137
	v_mul_f32_e32 v136, v136, v136
	v_mul_f32_e32 v137, v137, v137
	v_lshlrev_b32_e32 v192, 16, v138
	v_and_b32_e32 v138, 0xffff0000, v138
	v_lshlrev_b32_e32 v193, 16, v139
	v_and_b32_e32 v139, 0xffff0000, v139
	v_fmac_f32_e32 v136, v142, v142
	v_fmac_f32_e32 v137, v143, v143
	v_add_f32_e32 v136, v136, v137
	v_mul_f32_e32 v137, v138, v138
	v_mul_f32_e32 v138, v139, v139
	v_fmac_f32_e32 v137, v192, v192
	v_fmac_f32_e32 v138, v193, v193
	v_add_f32_e32 v137, v137, v138
	v_add_f32_e32 v192, v136, v137
	s_waitcnt vmcnt(15)
	v_lshlrev_b32_e32 v136, 16, v188
	v_and_b32_e32 v137, 0xffff0000, v188
	v_lshlrev_b32_e32 v138, 16, v189
	v_and_b32_e32 v139, 0xffff0000, v189
	v_lshlrev_b32_e32 v142, 16, v190
	v_and_b32_e32 v143, 0xffff0000, v190
	v_lshlrev_b32_e32 v188, 16, v191
	v_and_b32_e32 v189, 0xffff0000, v191
	v_pk_fma_f32 v[130:131], v[130:131], v[232:233], v[138:139] op_sel_hi:[1,0,1]
	v_pk_fma_f32 v[128:129], v[128:129], v[232:233], v[136:137] op_sel_hi:[1,0,1]
	v_pk_fma_f32 v[136:137], v[126:127], v[232:233], v[188:189] op_sel_hi:[1,0,1]
	v_pk_fma_f32 v[126:127], v[124:125], v[232:233], v[142:143] op_sel_hi:[1,0,1]
	v_cvt_pk_bf16_f32 v124, v128, v129
	v_cvt_pk_bf16_f32 v125, v130, v131
	v_cvt_pk_bf16_f32 v126, v126, v127
	v_cvt_pk_bf16_f32 v127, v136, v137
	global_store_dwordx4 v[140:141], v[124:127], off offset:256 nt
	v_lshlrev_b32_e32 v128, 16, v124
	v_lshlrev_b32_e32 v129, 16, v125
	v_and_b32_e32 v124, 0xffff0000, v124
	v_and_b32_e32 v125, 0xffff0000, v125
	v_mul_f32_e32 v124, v124, v124
	v_mul_f32_e32 v125, v125, v125
	v_lshlrev_b32_e32 v130, 16, v126
	v_and_b32_e32 v126, 0xffff0000, v126
	v_lshlrev_b32_e32 v131, 16, v127
	v_and_b32_e32 v127, 0xffff0000, v127
	v_fmac_f32_e32 v124, v128, v128
	v_fmac_f32_e32 v125, v129, v129
	v_add_f32_e32 v124, v124, v125
	v_mul_f32_e32 v125, v126, v126
	v_mul_f32_e32 v126, v127, v127
	v_fmac_f32_e32 v125, v130, v130
	v_fmac_f32_e32 v126, v131, v131
	v_add_f32_e32 v125, v125, v126
	v_add_f32_e32 v124, v124, v125
	v_add_f32_e32 v124, v192, v124
	ds_bpermute_b32 v125, v240, v124
	s_waitcnt lgkmcnt(0)
	v_add_f32_e32 v124, v124, v125
	ds_bpermute_b32 v125, v241, v124
	s_and_saveexec_b64 s[4:5], vcc
	v_readlane_b32 s74, v255, 38
	s_cbranch_execz .LBB0_1464
	v_lshlrev_b64 v[126:127], 6, v[216:217]
	v_lshl_add_u64 v[126:127], s[18:19], 0, v[126:127]
	v_lshl_add_u64 v[126:127], s[48:49], 2, v[126:127]
	s_lshl_b32 s56, s59, 2
	v_lshl_add_u64 v[126:127], v[126:127], 0, s[56:57]
	s_waitcnt lgkmcnt(0)
	v_add_f32_e32 v124, v124, v125
	global_store_dword v[126:127], v124, off
.LBB0_1464:
	s_or_b64 exec, exec, s[4:5]
	v_mul_f32_e32 v124, v246, v246
	s_waitcnt vmcnt(15)
	v_lshlrev_b32_e32 v126, 16, v184
	v_and_b32_e32 v127, 0xffff0000, v184
	v_lshlrev_b32_e32 v128, 16, v185
	v_and_b32_e32 v129, 0xffff0000, v185
	v_lshlrev_b32_e32 v130, 16, v186
	v_and_b32_e32 v131, 0xffff0000, v186
	v_lshlrev_b32_e32 v136, 16, v187
	v_and_b32_e32 v137, 0xffff0000, v187
	s_waitcnt lgkmcnt(0)
	v_pk_fma_f32 v[116:117], v[116:117], v[124:125], v[126:127] op_sel_hi:[1,0,1]
	v_pk_fma_f32 v[118:119], v[118:119], v[124:125], v[128:129] op_sel_hi:[1,0,1]
	v_pk_fma_f32 v[126:127], v[110:111], v[124:125], v[136:137] op_sel_hi:[1,0,1]
	v_pk_fma_f32 v[110:111], v[108:109], v[124:125], v[130:131] op_sel_hi:[1,0,1]
	v_cvt_pk_bf16_f32 v108, v116, v117
	v_cvt_pk_bf16_f32 v109, v118, v119
	v_and_b32_e32 v117, 0xffff0000, v108
	v_lshlrev_b32_e32 v116, 16, v108
	v_and_b32_e32 v119, 0xffff0000, v109
	v_mul_f32_e32 v117, v117, v117
	v_cvt_pk_bf16_f32 v110, v110, v111
	v_cvt_pk_bf16_f32 v111, v126, v127
	v_lshlrev_b32_e32 v118, 16, v109
	v_fmac_f32_e32 v117, v116, v116
	v_mul_f32_e32 v116, v119, v119
	v_and_b32_e32 v126, 0xffff0000, v110
	v_and_b32_e32 v128, 0xffff0000, v111
	v_fmac_f32_e32 v116, v118, v118
	v_lshlrev_b32_e32 v125, 16, v110
	v_lshlrev_b32_e32 v127, 16, v111
	v_add_f32_e32 v116, v117, v116
	v_mul_f32_e32 v117, v126, v126
	v_mul_f32_e32 v118, v128, v128
	v_fmac_f32_e32 v117, v125, v125
	v_fmac_f32_e32 v118, v127, v127
	v_add_f32_e32 v117, v117, v118
	v_add_f32_e32 v125, v116, v117
	s_waitcnt vmcnt(14)
	v_lshlrev_b32_e32 v116, 16, v180
	v_and_b32_e32 v117, 0xffff0000, v180
	v_lshlrev_b32_e32 v118, 16, v181
	v_and_b32_e32 v119, 0xffff0000, v181
	v_lshlrev_b32_e32 v126, 16, v182
	v_and_b32_e32 v127, 0xffff0000, v182
	v_lshlrev_b32_e32 v128, 16, v183
	v_and_b32_e32 v129, 0xffff0000, v183
	v_pk_fma_f32 v[104:105], v[104:105], v[124:125], v[116:117] op_sel_hi:[1,0,1]
	v_pk_fma_f32 v[106:107], v[106:107], v[124:125], v[118:119] op_sel_hi:[1,0,1]
	v_pk_fma_f32 v[116:117], v[102:103], v[124:125], v[128:129] op_sel_hi:[1,0,1]
	v_pk_fma_f32 v[100:101], v[100:101], v[124:125], v[126:127] op_sel_hi:[1,0,1]
	v_cvt_pk_bf16_f32 v102, v104, v105
	v_cvt_pk_bf16_f32 v103, v106, v107
	v_cvt_pk_bf16_f32 v104, v100, v101
	v_and_b32_e32 v101, 0xffff0000, v102
	v_lshlrev_b32_e32 v100, 16, v102
	v_and_b32_e32 v107, 0xffff0000, v103
	v_mul_f32_e32 v101, v101, v101
	v_cvt_pk_bf16_f32 v105, v116, v117
	v_lshlrev_b32_e32 v106, 16, v103
	v_fmac_f32_e32 v101, v100, v100
	v_mul_f32_e32 v100, v107, v107
	v_and_b32_e32 v117, 0xffff0000, v104
	v_and_b32_e32 v119, 0xffff0000, v105
	v_fmac_f32_e32 v100, v106, v106
	v_lshlrev_b32_e32 v116, 16, v104
	v_lshlrev_b32_e32 v118, 16, v105
	v_add_f32_e32 v100, v101, v100
	v_mul_f32_e32 v101, v117, v117
	v_mul_f32_e32 v106, v119, v119
	v_fmac_f32_e32 v101, v116, v116
	v_fmac_f32_e32 v106, v118, v118
	v_add_f32_e32 v101, v101, v106
	v_add_f32_e32 v100, v100, v101
	v_add_f32_e32 v100, v125, v100
	ds_bpermute_b32 v101, v240, v100
	v_lshl_add_u64 v[106:107], s[14:15], 0, v[230:231]
	v_lshl_add_u64 v[106:107], v[214:215], 1, v[106:107]
	global_store_dwordx4 v[106:107], v[108:111], off nt
	global_store_dwordx4 v[106:107], v[102:105], off offset:256 nt
	s_waitcnt lgkmcnt(0)
	v_add_f32_e32 v100, v100, v101
	ds_bpermute_b32 v101, v241, v100
	s_and_saveexec_b64 s[4:5], vcc
	s_cbranch_execz .LBB0_1466
	v_lshlrev_b64 v[102:103], 6, v[226:227]
	v_lshl_add_u64 v[102:103], s[18:19], 0, v[102:103]
	v_lshl_add_u64 v[102:103], s[48:49], 2, v[102:103]
	s_lshl_b32 s56, s59, 2
	v_lshl_add_u64 v[102:103], v[102:103], 0, s[56:57]
	s_waitcnt lgkmcnt(0)
	v_add_f32_e32 v100, v100, v101
	global_store_dword v[102:103], v100, off
.LBB0_1466:
	s_or_b64 exec, exec, s[4:5]
	v_mul_f32_e32 v100, v245, v245
	s_waitcnt vmcnt(15)
	v_lshlrev_b32_e32 v102, 16, v176
	v_and_b32_e32 v103, 0xffff0000, v176
	v_lshlrev_b32_e32 v104, 16, v177
	v_and_b32_e32 v105, 0xffff0000, v177
	v_lshlrev_b32_e32 v106, 16, v178
	v_and_b32_e32 v107, 0xffff0000, v178
	v_lshlrev_b32_e32 v108, 16, v179
	v_and_b32_e32 v109, 0xffff0000, v179
	s_waitcnt lgkmcnt(0)
	v_pk_fma_f32 v[96:97], v[96:97], v[100:101], v[102:103] op_sel_hi:[1,0,1]
	v_pk_fma_f32 v[98:99], v[98:99], v[100:101], v[104:105] op_sel_hi:[1,0,1]
	v_pk_fma_f32 v[102:103], v[94:95], v[100:101], v[108:109] op_sel_hi:[1,0,1]
	v_pk_fma_f32 v[94:95], v[92:93], v[100:101], v[106:107] op_sel_hi:[1,0,1]
	v_cvt_pk_bf16_f32 v92, v96, v97
	v_cvt_pk_bf16_f32 v93, v98, v99
	v_and_b32_e32 v97, 0xffff0000, v92
	v_lshlrev_b32_e32 v96, 16, v92
	v_and_b32_e32 v99, 0xffff0000, v93
	v_mul_f32_e32 v97, v97, v97
	v_cvt_pk_bf16_f32 v94, v94, v95
	v_cvt_pk_bf16_f32 v95, v102, v103
	v_lshlrev_b32_e32 v98, 16, v93
	v_fmac_f32_e32 v97, v96, v96
	v_mul_f32_e32 v96, v99, v99
	v_and_b32_e32 v102, 0xffff0000, v94
	v_and_b32_e32 v104, 0xffff0000, v95
	v_fmac_f32_e32 v96, v98, v98
	v_lshlrev_b32_e32 v101, 16, v94
	v_lshlrev_b32_e32 v103, 16, v95
	v_add_f32_e32 v96, v97, v96
	v_mul_f32_e32 v97, v102, v102
	v_mul_f32_e32 v98, v104, v104
	v_fmac_f32_e32 v97, v101, v101
	v_fmac_f32_e32 v98, v103, v103
	v_add_f32_e32 v97, v97, v98
	v_add_f32_e32 v101, v96, v97
	s_waitcnt vmcnt(14)
	v_lshlrev_b32_e32 v96, 16, v172
	v_and_b32_e32 v97, 0xffff0000, v172
	v_lshlrev_b32_e32 v98, 16, v173
	v_and_b32_e32 v99, 0xffff0000, v173
	v_lshlrev_b32_e32 v102, 16, v174
	v_and_b32_e32 v103, 0xffff0000, v174
	v_lshlrev_b32_e32 v104, 16, v175
	v_and_b32_e32 v105, 0xffff0000, v175
	v_pk_fma_f32 v[88:89], v[88:89], v[100:101], v[96:97] op_sel_hi:[1,0,1]
	v_pk_fma_f32 v[90:91], v[90:91], v[100:101], v[98:99] op_sel_hi:[1,0,1]
	v_pk_fma_f32 v[96:97], v[86:87], v[100:101], v[104:105] op_sel_hi:[1,0,1]
	v_pk_fma_f32 v[84:85], v[84:85], v[100:101], v[102:103] op_sel_hi:[1,0,1]
	v_cvt_pk_bf16_f32 v86, v88, v89
	v_cvt_pk_bf16_f32 v87, v90, v91
	v_cvt_pk_bf16_f32 v88, v84, v85
	v_and_b32_e32 v85, 0xffff0000, v86
	v_lshlrev_b32_e32 v84, 16, v86
	v_and_b32_e32 v91, 0xffff0000, v87
	v_mul_f32_e32 v85, v85, v85
	v_cvt_pk_bf16_f32 v89, v96, v97
	v_lshlrev_b32_e32 v90, 16, v87
	v_fmac_f32_e32 v85, v84, v84
	v_mul_f32_e32 v84, v91, v91
	v_and_b32_e32 v97, 0xffff0000, v88
	v_and_b32_e32 v99, 0xffff0000, v89
	v_fmac_f32_e32 v84, v90, v90
	v_lshlrev_b32_e32 v96, 16, v88
	v_lshlrev_b32_e32 v98, 16, v89
	v_add_f32_e32 v84, v85, v84
	v_mul_f32_e32 v85, v97, v97
	v_mul_f32_e32 v90, v99, v99
	v_fmac_f32_e32 v85, v96, v96
	v_fmac_f32_e32 v90, v98, v98
	v_add_f32_e32 v85, v85, v90
	v_add_f32_e32 v84, v84, v85
	v_add_f32_e32 v84, v101, v84
	ds_bpermute_b32 v85, v240, v84
	v_lshl_add_u64 v[90:91], s[14:15], 0, v[228:229]
	v_lshl_add_u64 v[90:91], v[214:215], 1, v[90:91]
	global_store_dwordx4 v[90:91], v[92:95], off nt
	global_store_dwordx4 v[90:91], v[86:89], off offset:256 nt
	s_waitcnt lgkmcnt(0)
	v_add_f32_e32 v84, v84, v85
	ds_bpermute_b32 v85, v241, v84
	s_and_saveexec_b64 s[4:5], vcc
	s_mov_b32 s78, 0xa000
	s_mov_b32 s77, 0xc000
	s_mov_b32 s76, 0xe000
	s_movk_i32 s75, 0x3400
	s_cbranch_execz .LBB0_1468
	v_lshlrev_b64 v[86:87], 6, v[222:223]
	v_lshl_add_u64 v[86:87], s[18:19], 0, v[86:87]
	v_lshl_add_u64 v[86:87], s[48:49], 2, v[86:87]
	s_lshl_b32 s56, s59, 2
	v_lshl_add_u64 v[86:87], v[86:87], 0, s[56:57]
	s_waitcnt lgkmcnt(0)
	v_add_f32_e32 v84, v84, v85
	global_store_dword v[86:87], v84, off
.LBB0_1468:
	s_or_b64 exec, exec, s[4:5]
	v_mul_f32_e32 v84, v244, v244
	s_waitcnt vmcnt(15)
	v_lshlrev_b32_e32 v86, 16, v168
	v_and_b32_e32 v87, 0xffff0000, v168
	v_lshlrev_b32_e32 v88, 16, v169
	v_and_b32_e32 v89, 0xffff0000, v169
	v_lshlrev_b32_e32 v90, 16, v170
	v_and_b32_e32 v91, 0xffff0000, v170
	v_lshlrev_b32_e32 v92, 16, v171
	v_and_b32_e32 v93, 0xffff0000, v171
	s_waitcnt lgkmcnt(0)
	v_pk_fma_f32 v[80:81], v[80:81], v[84:85], v[86:87] op_sel_hi:[1,0,1]
	v_pk_fma_f32 v[82:83], v[82:83], v[84:85], v[88:89] op_sel_hi:[1,0,1]
	v_pk_fma_f32 v[86:87], v[78:79], v[84:85], v[92:93] op_sel_hi:[1,0,1]
	v_pk_fma_f32 v[78:79], v[76:77], v[84:85], v[90:91] op_sel_hi:[1,0,1]
	v_cvt_pk_bf16_f32 v76, v80, v81
	v_cvt_pk_bf16_f32 v77, v82, v83
	v_and_b32_e32 v81, 0xffff0000, v76
	v_lshlrev_b32_e32 v80, 16, v76
	v_and_b32_e32 v83, 0xffff0000, v77
	v_mul_f32_e32 v81, v81, v81
	v_cvt_pk_bf16_f32 v78, v78, v79
	v_cvt_pk_bf16_f32 v79, v86, v87
	v_lshlrev_b32_e32 v82, 16, v77
	v_fmac_f32_e32 v81, v80, v80
	v_mul_f32_e32 v80, v83, v83
	v_and_b32_e32 v86, 0xffff0000, v78
	v_and_b32_e32 v88, 0xffff0000, v79
	v_fmac_f32_e32 v80, v82, v82
	v_lshlrev_b32_e32 v85, 16, v78
	v_lshlrev_b32_e32 v87, 16, v79
	v_add_f32_e32 v80, v81, v80
	v_mul_f32_e32 v81, v86, v86
	v_mul_f32_e32 v82, v88, v88
	v_fmac_f32_e32 v81, v85, v85
	v_fmac_f32_e32 v82, v87, v87
	v_add_f32_e32 v81, v81, v82
	v_add_f32_e32 v85, v80, v81
	s_waitcnt vmcnt(14)
	v_lshlrev_b32_e32 v80, 16, v164
	v_and_b32_e32 v81, 0xffff0000, v164
	v_lshlrev_b32_e32 v82, 16, v165
	v_and_b32_e32 v83, 0xffff0000, v165
	v_lshlrev_b32_e32 v86, 16, v166
	v_and_b32_e32 v87, 0xffff0000, v166
	v_lshlrev_b32_e32 v88, 16, v167
	v_and_b32_e32 v89, 0xffff0000, v167
	v_pk_fma_f32 v[72:73], v[72:73], v[84:85], v[80:81] op_sel_hi:[1,0,1]
	v_pk_fma_f32 v[74:75], v[74:75], v[84:85], v[82:83] op_sel_hi:[1,0,1]
	v_pk_fma_f32 v[80:81], v[70:71], v[84:85], v[88:89] op_sel_hi:[1,0,1]
	v_pk_fma_f32 v[68:69], v[68:69], v[84:85], v[86:87] op_sel_hi:[1,0,1]
	v_cvt_pk_bf16_f32 v70, v72, v73
	v_cvt_pk_bf16_f32 v71, v74, v75
	v_cvt_pk_bf16_f32 v72, v68, v69
	v_and_b32_e32 v69, 0xffff0000, v70
	v_lshlrev_b32_e32 v68, 16, v70
	v_and_b32_e32 v75, 0xffff0000, v71
	v_mul_f32_e32 v69, v69, v69
	v_cvt_pk_bf16_f32 v73, v80, v81
	v_lshlrev_b32_e32 v74, 16, v71
	v_fmac_f32_e32 v69, v68, v68
	v_mul_f32_e32 v68, v75, v75
	v_and_b32_e32 v81, 0xffff0000, v72
	v_and_b32_e32 v83, 0xffff0000, v73
	v_fmac_f32_e32 v68, v74, v74
	v_lshlrev_b32_e32 v80, 16, v72
	v_lshlrev_b32_e32 v82, 16, v73
	v_add_f32_e32 v68, v69, v68
	v_mul_f32_e32 v69, v81, v81
	v_mul_f32_e32 v74, v83, v83
	v_fmac_f32_e32 v69, v80, v80
	v_fmac_f32_e32 v74, v82, v82
	v_add_f32_e32 v69, v69, v74
	v_add_f32_e32 v68, v68, v69
	v_add_f32_e32 v68, v85, v68
	ds_bpermute_b32 v69, v240, v68
	v_lshl_add_u64 v[74:75], s[14:15], 0, v[224:225]
	v_lshl_add_u64 v[74:75], v[214:215], 1, v[74:75]
	global_store_dwordx4 v[74:75], v[76:79], off nt
	global_store_dwordx4 v[74:75], v[70:73], off offset:256 nt
	s_waitcnt lgkmcnt(0)
	v_add_f32_e32 v68, v68, v69
	ds_bpermute_b32 v69, v241, v68
	s_and_saveexec_b64 s[4:5], vcc
	s_cbranch_execz .LBB0_1470
	v_lshlrev_b64 v[70:71], 6, v[220:221]
	v_lshl_add_u64 v[70:71], s[18:19], 0, v[70:71]
	v_lshl_add_u64 v[70:71], s[48:49], 2, v[70:71]
	s_lshl_b32 s56, s59, 2
	v_lshl_add_u64 v[70:71], v[70:71], 0, s[56:57]
	s_waitcnt lgkmcnt(0)
	v_add_f32_e32 v68, v68, v69
	global_store_dword v[70:71], v68, off
.LBB0_1470:
	s_or_b64 exec, exec, s[4:5]
	v_mul_f32_e32 v68, v243, v243
	s_waitcnt vmcnt(15)
	v_lshlrev_b32_e32 v70, 16, v160
	v_and_b32_e32 v71, 0xffff0000, v160
	v_lshlrev_b32_e32 v72, 16, v161
	v_and_b32_e32 v73, 0xffff0000, v161
	v_lshlrev_b32_e32 v74, 16, v162
	v_and_b32_e32 v75, 0xffff0000, v162
	v_lshlrev_b32_e32 v76, 16, v163
	v_and_b32_e32 v77, 0xffff0000, v163
	s_waitcnt lgkmcnt(0)
	v_pk_fma_f32 v[64:65], v[64:65], v[68:69], v[70:71] op_sel_hi:[1,0,1]
	v_pk_fma_f32 v[66:67], v[66:67], v[68:69], v[72:73] op_sel_hi:[1,0,1]
	v_pk_fma_f32 v[70:71], v[62:63], v[68:69], v[76:77] op_sel_hi:[1,0,1]
	v_pk_fma_f32 v[62:63], v[60:61], v[68:69], v[74:75] op_sel_hi:[1,0,1]
	v_cvt_pk_bf16_f32 v60, v64, v65
	v_cvt_pk_bf16_f32 v61, v66, v67
	v_and_b32_e32 v65, 0xffff0000, v60
	v_lshlrev_b32_e32 v64, 16, v60
	v_and_b32_e32 v67, 0xffff0000, v61
	v_mul_f32_e32 v65, v65, v65
	v_cvt_pk_bf16_f32 v62, v62, v63
	v_cvt_pk_bf16_f32 v63, v70, v71
	v_lshlrev_b32_e32 v66, 16, v61
	v_fmac_f32_e32 v65, v64, v64
	v_mul_f32_e32 v64, v67, v67
	v_and_b32_e32 v70, 0xffff0000, v62
	v_and_b32_e32 v72, 0xffff0000, v63
	v_fmac_f32_e32 v64, v66, v66
	v_lshlrev_b32_e32 v69, 16, v62
	v_lshlrev_b32_e32 v71, 16, v63
	v_add_f32_e32 v64, v65, v64
	v_mul_f32_e32 v65, v70, v70
	v_mul_f32_e32 v66, v72, v72
	v_fmac_f32_e32 v65, v69, v69
	v_fmac_f32_e32 v66, v71, v71
	v_add_f32_e32 v65, v65, v66
	v_add_f32_e32 v69, v64, v65
	s_waitcnt vmcnt(14)
	v_lshlrev_b32_e32 v64, 16, v156
	v_and_b32_e32 v65, 0xffff0000, v156
	v_lshlrev_b32_e32 v66, 16, v157
	v_and_b32_e32 v67, 0xffff0000, v157
	v_lshlrev_b32_e32 v70, 16, v158
	v_and_b32_e32 v71, 0xffff0000, v158
	v_lshlrev_b32_e32 v72, 16, v159
	v_and_b32_e32 v73, 0xffff0000, v159
	v_pk_fma_f32 v[56:57], v[56:57], v[68:69], v[64:65] op_sel_hi:[1,0,1]
	v_pk_fma_f32 v[58:59], v[58:59], v[68:69], v[66:67] op_sel_hi:[1,0,1]
	v_pk_fma_f32 v[64:65], v[54:55], v[68:69], v[72:73] op_sel_hi:[1,0,1]
	v_pk_fma_f32 v[52:53], v[52:53], v[68:69], v[70:71] op_sel_hi:[1,0,1]
	v_cvt_pk_bf16_f32 v54, v56, v57
	v_cvt_pk_bf16_f32 v55, v58, v59
	v_cvt_pk_bf16_f32 v56, v52, v53
	v_and_b32_e32 v53, 0xffff0000, v54
	v_lshlrev_b32_e32 v52, 16, v54
	v_and_b32_e32 v59, 0xffff0000, v55
	v_mul_f32_e32 v53, v53, v53
	v_cvt_pk_bf16_f32 v57, v64, v65
	v_lshlrev_b32_e32 v58, 16, v55
	v_fmac_f32_e32 v53, v52, v52
	v_mul_f32_e32 v52, v59, v59
	v_and_b32_e32 v65, 0xffff0000, v56
	v_and_b32_e32 v67, 0xffff0000, v57
	v_fmac_f32_e32 v52, v58, v58
	v_lshlrev_b32_e32 v64, 16, v56
	v_lshlrev_b32_e32 v66, 16, v57
	v_add_f32_e32 v52, v53, v52
	v_mul_f32_e32 v53, v65, v65
	v_mul_f32_e32 v58, v67, v67
	v_fmac_f32_e32 v53, v64, v64
	v_fmac_f32_e32 v58, v66, v66
	v_add_f32_e32 v53, v53, v58
	v_add_f32_e32 v52, v52, v53
	v_add_f32_e32 v52, v69, v52
	ds_bpermute_b32 v53, v240, v52
	v_lshlrev_b64 v[58:59], 10, v[218:219]
	v_lshl_add_u64 v[58:59], v[58:59], 1, s[14:15]
	v_lshl_add_u64 v[58:59], v[214:215], 1, v[58:59]
	global_store_dwordx4 v[58:59], v[60:63], off nt
	global_store_dwordx4 v[58:59], v[54:57], off offset:256 nt
	s_waitcnt lgkmcnt(0)
	v_add_f32_e32 v52, v52, v53
	ds_bpermute_b32 v53, v241, v52
	s_and_saveexec_b64 s[4:5], vcc
	s_cbranch_execz .LBB0_1472
	v_lshlrev_b64 v[54:55], 6, v[218:219]
	v_lshl_add_u64 v[54:55], s[18:19], 0, v[54:55]
	v_lshl_add_u64 v[54:55], s[48:49], 2, v[54:55]
	s_lshl_b32 s56, s59, 2
	v_lshl_add_u64 v[54:55], v[54:55], 0, s[56:57]
	s_waitcnt lgkmcnt(0)
	v_add_f32_e32 v52, v52, v53
	global_store_dword v[54:55], v52, off
.LBB0_1472:
	s_or_b64 exec, exec, s[4:5]
	v_mul_f32_e32 v52, v242, v242
	s_waitcnt vmcnt(15)
	v_lshlrev_b32_e32 v54, 16, v152
	v_and_b32_e32 v55, 0xffff0000, v152
	v_lshlrev_b32_e32 v56, 16, v153
	v_and_b32_e32 v57, 0xffff0000, v153
	v_lshlrev_b32_e32 v58, 16, v154
	v_and_b32_e32 v59, 0xffff0000, v154
	v_lshlrev_b32_e32 v60, 16, v155
	v_and_b32_e32 v61, 0xffff0000, v155
	s_waitcnt lgkmcnt(0)
	v_pk_fma_f32 v[48:49], v[48:49], v[52:53], v[54:55] op_sel_hi:[1,0,1]
	v_pk_fma_f32 v[50:51], v[50:51], v[52:53], v[56:57] op_sel_hi:[1,0,1]
	v_pk_fma_f32 v[54:55], v[46:47], v[52:53], v[60:61] op_sel_hi:[1,0,1]
	v_pk_fma_f32 v[46:47], v[44:45], v[52:53], v[58:59] op_sel_hi:[1,0,1]
	v_cvt_pk_bf16_f32 v44, v48, v49
	v_cvt_pk_bf16_f32 v45, v50, v51
	v_and_b32_e32 v49, 0xffff0000, v44
	v_lshlrev_b32_e32 v48, 16, v44
	v_and_b32_e32 v51, 0xffff0000, v45
	v_mul_f32_e32 v49, v49, v49
	v_cvt_pk_bf16_f32 v46, v46, v47
	v_cvt_pk_bf16_f32 v47, v54, v55
	v_lshlrev_b32_e32 v50, 16, v45
	v_fmac_f32_e32 v49, v48, v48
	v_mul_f32_e32 v48, v51, v51
	v_and_b32_e32 v54, 0xffff0000, v46
	v_and_b32_e32 v56, 0xffff0000, v47
	v_fmac_f32_e32 v48, v50, v50
	v_lshlrev_b32_e32 v53, 16, v46
	v_lshlrev_b32_e32 v55, 16, v47
	v_add_f32_e32 v48, v49, v48
	v_mul_f32_e32 v49, v54, v54
	v_mul_f32_e32 v50, v56, v56
	v_fmac_f32_e32 v49, v53, v53
	v_fmac_f32_e32 v50, v55, v55
	v_add_f32_e32 v49, v49, v50
	v_add_f32_e32 v53, v48, v49
	s_waitcnt vmcnt(14)
	v_lshlrev_b32_e32 v48, 16, v148
	v_and_b32_e32 v49, 0xffff0000, v148
	v_lshlrev_b32_e32 v50, 16, v149
	v_and_b32_e32 v51, 0xffff0000, v149
	v_lshlrev_b32_e32 v54, 16, v150
	v_and_b32_e32 v55, 0xffff0000, v150
	v_pk_fma_f32 v[40:41], v[40:41], v[52:53], v[48:49] op_sel_hi:[1,0,1]
	v_lshlrev_b32_e32 v56, 16, v151
	v_and_b32_e32 v57, 0xffff0000, v151
	v_pk_fma_f32 v[42:43], v[42:43], v[52:53], v[50:51] op_sel_hi:[1,0,1]
	v_pk_fma_f32 v[36:37], v[36:37], v[52:53], v[54:55] op_sel_hi:[1,0,1]
	v_cvt_pk_bf16_f32 v40, v40, v41
	v_pk_fma_f32 v[38:39], v[38:39], v[52:53], v[56:57] op_sel_hi:[1,0,1]
	v_cvt_pk_bf16_f32 v41, v42, v43
	v_cvt_pk_bf16_f32 v42, v36, v37
	v_and_b32_e32 v37, 0xffff0000, v40
	v_cvt_pk_bf16_f32 v43, v38, v39
	v_lshlrev_b32_e32 v36, 16, v40
	v_and_b32_e32 v39, 0xffff0000, v41
	v_mul_f32_e32 v37, v37, v37
	v_lshlrev_b32_e32 v38, 16, v41
	v_fmac_f32_e32 v37, v36, v36
	v_mul_f32_e32 v36, v39, v39
	v_and_b32_e32 v49, 0xffff0000, v42
	v_and_b32_e32 v51, 0xffff0000, v43
	v_fmac_f32_e32 v36, v38, v38
	v_lshlrev_b32_e32 v48, 16, v42
	v_lshlrev_b32_e32 v50, 16, v43
	v_add_f32_e32 v36, v37, v36
	v_mul_f32_e32 v37, v49, v49
	v_mul_f32_e32 v38, v51, v51
	v_fmac_f32_e32 v37, v48, v48
	v_fmac_f32_e32 v38, v50, v50
	v_add_f32_e32 v37, v37, v38
	v_add_f32_e32 v36, v36, v37
	v_add_f32_e32 v38, v53, v36
	ds_bpermute_b32 v39, v240, v38
	v_add_u32_e32 v36, 0x90, v216
	v_ashrrev_i32_e32 v37, 31, v36
	v_lshlrev_b64 v[48:49], 11, v[36:37]
	v_lshl_add_u64 v[48:49], s[14:15], 0, v[48:49]
	s_waitcnt lgkmcnt(0)
	v_add_f32_e32 v38, v38, v39
	ds_bpermute_b32 v39, v241, v38
	v_lshl_add_u64 v[48:49], v[214:215], 1, v[48:49]
	global_store_dwordx4 v[48:49], v[44:47], off nt
	global_store_dwordx4 v[48:49], v[40:43], off offset:256 nt
	s_and_saveexec_b64 s[4:5], vcc
	s_cbranch_execz .LBB0_1474
	v_lshlrev_b64 v[36:37], 6, v[36:37]
	v_lshl_add_u64 v[36:37], s[18:19], 0, v[36:37]
	v_lshl_add_u64 v[36:37], s[48:49], 2, v[36:37]
	s_lshl_b32 s56, s59, 2
	v_lshl_add_u64 v[36:37], v[36:37], 0, s[56:57]
	s_waitcnt lgkmcnt(0)
	v_add_f32_e32 v38, v38, v39
	global_store_dword v[36:37], v38, off
.LBB0_1474:
	s_or_b64 exec, exec, s[4:5]
	v_mul_f32_e32 v36, v239, v239
	s_waitcnt vmcnt(15)
	v_lshlrev_b32_e32 v38, 16, v144
	s_waitcnt lgkmcnt(0)
	v_and_b32_e32 v39, 0xffff0000, v144
	v_lshlrev_b32_e32 v40, 16, v145
	v_and_b32_e32 v41, 0xffff0000, v145
	v_lshlrev_b32_e32 v42, 16, v146
	v_and_b32_e32 v43, 0xffff0000, v146
	v_lshlrev_b32_e32 v44, 16, v147
	v_and_b32_e32 v45, 0xffff0000, v147
	v_pk_fma_f32 v[32:33], v[32:33], v[36:37], v[38:39] op_sel_hi:[1,0,1]
	v_pk_fma_f32 v[34:35], v[34:35], v[36:37], v[40:41] op_sel_hi:[1,0,1]
	v_pk_fma_f32 v[38:39], v[30:31], v[36:37], v[44:45] op_sel_hi:[1,0,1]
	v_pk_fma_f32 v[30:31], v[28:29], v[36:37], v[42:43] op_sel_hi:[1,0,1]
	v_cvt_pk_bf16_f32 v28, v32, v33
	v_cvt_pk_bf16_f32 v29, v34, v35
	v_and_b32_e32 v33, 0xffff0000, v28
	v_lshlrev_b32_e32 v32, 16, v28
	v_and_b32_e32 v35, 0xffff0000, v29
	v_mul_f32_e32 v33, v33, v33
	v_cvt_pk_bf16_f32 v30, v30, v31
	v_cvt_pk_bf16_f32 v31, v38, v39
	v_lshlrev_b32_e32 v34, 16, v29
	v_fmac_f32_e32 v33, v32, v32
	v_mul_f32_e32 v32, v35, v35
	v_and_b32_e32 v38, 0xffff0000, v30
	v_and_b32_e32 v40, 0xffff0000, v31
	v_fmac_f32_e32 v32, v34, v34
	v_lshlrev_b32_e32 v37, 16, v30
	v_lshlrev_b32_e32 v39, 16, v31
	v_add_f32_e32 v32, v33, v32
	v_mul_f32_e32 v33, v38, v38
	v_mul_f32_e32 v34, v40, v40
	v_fmac_f32_e32 v33, v37, v37
	v_fmac_f32_e32 v34, v39, v39
	v_add_f32_e32 v33, v33, v34
	v_add_f32_e32 v37, v32, v33
	s_waitcnt vmcnt(14)
	v_lshlrev_b32_e32 v32, 16, v132
	v_and_b32_e32 v33, 0xffff0000, v132
	v_lshlrev_b32_e32 v34, 16, v133
	v_and_b32_e32 v35, 0xffff0000, v133
	v_lshlrev_b32_e32 v38, 16, v134
	v_and_b32_e32 v39, 0xffff0000, v134
	v_pk_fma_f32 v[24:25], v[24:25], v[36:37], v[32:33] op_sel_hi:[1,0,1]
	v_lshlrev_b32_e32 v40, 16, v135
	v_and_b32_e32 v41, 0xffff0000, v135
	v_pk_fma_f32 v[26:27], v[26:27], v[36:37], v[34:35] op_sel_hi:[1,0,1]
	v_pk_fma_f32 v[20:21], v[20:21], v[36:37], v[38:39] op_sel_hi:[1,0,1]
	v_cvt_pk_bf16_f32 v24, v24, v25
	v_pk_fma_f32 v[22:23], v[22:23], v[36:37], v[40:41] op_sel_hi:[1,0,1]
	v_cvt_pk_bf16_f32 v25, v26, v27
	v_cvt_pk_bf16_f32 v26, v20, v21
	v_and_b32_e32 v21, 0xffff0000, v24
	v_cvt_pk_bf16_f32 v27, v22, v23
	v_lshlrev_b32_e32 v20, 16, v24
	v_and_b32_e32 v23, 0xffff0000, v25
	v_mul_f32_e32 v21, v21, v21
	v_lshlrev_b32_e32 v22, 16, v25
	v_fmac_f32_e32 v21, v20, v20
	v_mul_f32_e32 v20, v23, v23
	v_and_b32_e32 v33, 0xffff0000, v26
	v_and_b32_e32 v35, 0xffff0000, v27
	v_fmac_f32_e32 v20, v22, v22
	v_lshlrev_b32_e32 v32, 16, v26
	v_lshlrev_b32_e32 v34, 16, v27
	v_add_f32_e32 v20, v21, v20
	v_mul_f32_e32 v21, v33, v33
	v_mul_f32_e32 v22, v35, v35
	v_fmac_f32_e32 v21, v32, v32
	v_fmac_f32_e32 v22, v34, v34
	v_add_f32_e32 v21, v21, v22
	v_add_f32_e32 v20, v20, v21
	v_add_f32_e32 v22, v37, v20
	ds_bpermute_b32 v23, v240, v22
	v_add_u32_e32 v20, 0xa0, v216
	v_ashrrev_i32_e32 v21, 31, v20
	v_lshlrev_b64 v[32:33], 11, v[20:21]
	v_lshl_add_u64 v[32:33], s[14:15], 0, v[32:33]
	s_waitcnt lgkmcnt(0)
	v_add_f32_e32 v22, v22, v23
	ds_bpermute_b32 v23, v241, v22
	v_lshl_add_u64 v[32:33], v[214:215], 1, v[32:33]
	global_store_dwordx4 v[32:33], v[28:31], off nt
	global_store_dwordx4 v[32:33], v[24:27], off offset:256 nt
	s_and_saveexec_b64 s[4:5], vcc
	s_cbranch_execz .LBB0_1476
	v_lshlrev_b64 v[20:21], 6, v[20:21]
	v_lshl_add_u64 v[20:21], s[18:19], 0, v[20:21]
	v_lshl_add_u64 v[20:21], s[48:49], 2, v[20:21]
	s_lshl_b32 s56, s59, 2
	v_lshl_add_u64 v[20:21], v[20:21], 0, s[56:57]
	s_waitcnt lgkmcnt(0)
	v_add_f32_e32 v22, v22, v23
	global_store_dword v[20:21], v22, off
.LBB0_1476:
	s_or_b64 exec, exec, s[4:5]
	v_mul_f32_e32 v20, v238, v238
	s_waitcnt vmcnt(15)
	v_lshlrev_b32_e32 v22, 16, v120
	s_waitcnt lgkmcnt(0)
	v_and_b32_e32 v23, 0xffff0000, v120
	v_lshlrev_b32_e32 v24, 16, v121
	v_and_b32_e32 v25, 0xffff0000, v121
	v_lshlrev_b32_e32 v26, 16, v122
	v_and_b32_e32 v27, 0xffff0000, v122
	v_lshlrev_b32_e32 v28, 16, v123
	v_and_b32_e32 v29, 0xffff0000, v123
	v_pk_fma_f32 v[16:17], v[16:17], v[20:21], v[22:23] op_sel_hi:[1,0,1]
	v_pk_fma_f32 v[18:19], v[18:19], v[20:21], v[24:25] op_sel_hi:[1,0,1]
	v_pk_fma_f32 v[22:23], v[14:15], v[20:21], v[28:29] op_sel_hi:[1,0,1]
	v_pk_fma_f32 v[14:15], v[12:13], v[20:21], v[26:27] op_sel_hi:[1,0,1]
	v_cvt_pk_bf16_f32 v12, v16, v17
	v_cvt_pk_bf16_f32 v13, v18, v19
	v_and_b32_e32 v17, 0xffff0000, v12
	v_lshlrev_b32_e32 v16, 16, v12
	v_and_b32_e32 v19, 0xffff0000, v13
	v_mul_f32_e32 v17, v17, v17
	v_cvt_pk_bf16_f32 v14, v14, v15
	v_cvt_pk_bf16_f32 v15, v22, v23
	v_lshlrev_b32_e32 v18, 16, v13
	v_fmac_f32_e32 v17, v16, v16
	v_mul_f32_e32 v16, v19, v19
	v_and_b32_e32 v22, 0xffff0000, v14
	v_and_b32_e32 v24, 0xffff0000, v15
	v_fmac_f32_e32 v16, v18, v18
	v_lshlrev_b32_e32 v21, 16, v14
	v_lshlrev_b32_e32 v23, 16, v15
	v_add_f32_e32 v16, v17, v16
	v_mul_f32_e32 v17, v22, v22
	v_mul_f32_e32 v18, v24, v24
	v_fmac_f32_e32 v17, v21, v21
	v_fmac_f32_e32 v18, v23, v23
	v_add_f32_e32 v17, v17, v18
	v_add_f32_e32 v21, v16, v17
	s_waitcnt vmcnt(14)
	v_lshlrev_b32_e32 v16, 16, v112
	v_and_b32_e32 v17, 0xffff0000, v112
	v_lshlrev_b32_e32 v18, 16, v113
	v_and_b32_e32 v19, 0xffff0000, v113
	v_lshlrev_b32_e32 v22, 16, v114
	v_and_b32_e32 v23, 0xffff0000, v114
	v_pk_fma_f32 v[8:9], v[8:9], v[20:21], v[16:17] op_sel_hi:[1,0,1]
	v_lshlrev_b32_e32 v24, 16, v115
	v_and_b32_e32 v25, 0xffff0000, v115
	v_pk_fma_f32 v[10:11], v[10:11], v[20:21], v[18:19] op_sel_hi:[1,0,1]
	v_pk_fma_f32 v[4:5], v[4:5], v[20:21], v[22:23] op_sel_hi:[1,0,1]
	v_cvt_pk_bf16_f32 v8, v8, v9
	v_pk_fma_f32 v[6:7], v[6:7], v[20:21], v[24:25] op_sel_hi:[1,0,1]
	v_cvt_pk_bf16_f32 v9, v10, v11
	v_cvt_pk_bf16_f32 v10, v4, v5
	v_and_b32_e32 v5, 0xffff0000, v8
	v_cvt_pk_bf16_f32 v11, v6, v7
	v_lshlrev_b32_e32 v4, 16, v8
	v_and_b32_e32 v7, 0xffff0000, v9
	v_mul_f32_e32 v5, v5, v5
	v_lshlrev_b32_e32 v6, 16, v9
	v_fmac_f32_e32 v5, v4, v4
	v_mul_f32_e32 v4, v7, v7
	v_and_b32_e32 v17, 0xffff0000, v10
	v_and_b32_e32 v19, 0xffff0000, v11
	v_fmac_f32_e32 v4, v6, v6
	v_lshlrev_b32_e32 v16, 16, v10
	v_lshlrev_b32_e32 v18, 16, v11
	v_add_f32_e32 v4, v5, v4
	v_mul_f32_e32 v5, v17, v17
	v_mul_f32_e32 v6, v19, v19
	v_fmac_f32_e32 v5, v16, v16
	v_fmac_f32_e32 v6, v18, v18
	v_add_f32_e32 v5, v5, v6
	v_add_f32_e32 v4, v4, v5
	v_add_f32_e32 v6, v21, v4
	ds_bpermute_b32 v7, v240, v6
	v_add_u32_e32 v4, 0xb0, v216
	v_ashrrev_i32_e32 v5, 31, v4
	v_lshlrev_b64 v[16:17], 11, v[4:5]
	v_lshl_add_u64 v[16:17], s[14:15], 0, v[16:17]
	s_waitcnt lgkmcnt(0)
	v_add_f32_e32 v6, v6, v7
	ds_bpermute_b32 v7, v241, v6
	v_lshl_add_u64 v[16:17], v[214:215], 1, v[16:17]
	global_store_dwordx4 v[16:17], v[12:15], off nt
	global_store_dwordx4 v[16:17], v[8:11], off offset:256 nt
	s_and_saveexec_b64 s[4:5], vcc
	s_cbranch_execz .LBB0_1478
	v_lshlrev_b64 v[4:5], 6, v[4:5]
	v_lshl_add_u64 v[4:5], s[18:19], 0, v[4:5]
	v_lshl_add_u64 v[4:5], s[48:49], 2, v[4:5]
	s_lshl_b32 s56, s59, 2
	v_lshl_add_u64 v[4:5], v[4:5], 0, s[56:57]
	s_waitcnt lgkmcnt(0)
	v_add_f32_e32 v6, v6, v7
	global_store_dword v[4:5], v6, off
